# v18 plus loop-counter SALU of six K-loops moved from behind the last compute barrier to in front of the last load segment's closing wait
# speedup vs baseline: 1.0014x; 1.0014x over previous
.LBB0_261:
	s_nop 2
	ds_read_b128 v[0:3], v219
	ds_read_b128 v[4:7], v219 offset:1024
	ds_read_b128 v[8:11], v219 offset:2048
	ds_read_b128 v[12:15], v219 offset:3072
	ds_read_b128 v[16:19], v220
	ds_read_b128 v[20:23], v220 offset:1024
	ds_read_b128 v[24:27], v220 offset:2048
	ds_read_b128 v[28:31], v220 offset:3072
	ds_read_b128 v[32:35], v221
	ds_read_b128 v[36:39], v221 offset:1024
	ds_read_b128 v[40:43], v221 offset:2048
	ds_read_b128 v[44:47], v221 offset:3072
	ds_read_b128 v[48:51], v221 offset:4096
	ds_read_b128 v[52:55], v221 offset:5120
	ds_read_b128 v[56:59], v221 offset:6144
	ds_read_b128 v[60:63], v221 offset:7168
	s_add_u32 s8, s46, 0x100
	s_addc_u32 s9, s47, 0
	s_cmp_eq_u32 s76, 12
	s_cselect_b32 s52, s11, s8
	s_cselect_b32 s53, s7, s9
	s_cselect_b32 s48, s41, s77
	s_cselect_b32 s49, s39, s80
	s_add_u32 s12, s52, 0x80
	s_addc_u32 s13, s53, 0
	s_add_u32 s50, s48, 0x80
	s_addc_u32 s51, s49, 0
	s_add_u32 s46, s46, 0x40080
	s_addc_u32 s47, s47, 0
	s_add_i32 m0, s59, 0xc000
	s_nop 0
	global_load_lds_dwordx4 v215, s[46:47]
	s_nop 0
	s_add_i32 m0, s59, 0xe000
	s_nop 0
	global_load_lds_dwordx4 v217, s[46:47]
	s_waitcnt vmcnt(8) lgkmcnt(0)
	s_barrier
	v_mfma_i32_16x16x64_i8 v[172:175], v[0:3], v[48:51], v[172:175]
	v_mfma_i32_16x16x64_i8 v[168:171], v[8:11], v[48:51], v[168:171]
	v_mfma_i32_16x16x64_i8 v[152:155], v[8:11], v[56:59], v[152:155]
	v_mfma_i32_16x16x64_i8 v[156:159], v[0:3], v[56:59], v[156:159]
	v_mfma_i32_16x16x64_i8 v[64:67], v[0:3], v[32:35], v[204:207]
	v_mfma_i32_16x16x64_i8 v[76:79], v[8:11], v[32:35], v[200:203]
	v_mfma_i32_16x16x64_i8 v[92:95], v[8:11], v[40:43], v[184:187]
	v_mfma_i32_16x16x64_i8 v[80:83], v[0:3], v[40:43], v[188:191]
	v_mfma_i32_16x16x64_i8 v[172:175], v[4:7], v[52:55], v[172:175]
	v_mfma_i32_16x16x64_i8 v[168:171], v[12:15], v[52:55], v[168:171]
	v_mfma_i32_16x16x64_i8 v[152:155], v[12:15], v[60:63], v[152:155]
	v_mfma_i32_16x16x64_i8 v[156:159], v[4:7], v[60:63], v[156:159]
	v_mfma_i32_16x16x64_i8 v[64:67], v[4:7], v[36:39], v[64:67]
	v_mfma_i32_16x16x64_i8 v[76:79], v[12:15], v[36:39], v[76:79]
	v_mfma_i32_16x16x64_i8 v[92:95], v[12:15], v[44:47], v[92:95]
	v_mfma_i32_16x16x64_i8 v[80:83], v[4:7], v[44:47], v[80:83]
	v_mfma_i32_16x16x64_i8 v[184:187], v[16:19], v[32:35], v[196:199]
	v_mfma_i32_16x16x64_i8 v[32:35], v[24:27], v[32:35], v[192:195]
	v_mfma_i32_16x16x64_i8 v[196:199], v[20:23], v[36:39], v[184:187]
	v_mfma_i32_16x16x64_i8 v[32:35], v[28:31], v[36:39], v[32:35]
	v_mfma_i32_16x16x64_i8 v[36:39], v[16:19], v[40:43], v[180:183]
	v_mfma_i32_16x16x64_i8 v[40:43], v[24:27], v[40:43], v[176:179]
	v_mfma_i32_16x16x64_i8 v[36:39], v[20:23], v[44:47], v[36:39]
	v_mfma_i32_16x16x64_i8 v[40:43], v[28:31], v[44:47], v[40:43]
	v_mfma_i32_16x16x64_i8 v[44:47], v[16:19], v[48:51], v[164:167]
	v_mfma_i32_16x16x64_i8 v[48:51], v[24:27], v[48:51], v[160:163]
	v_mfma_i32_16x16x64_i8 v[44:47], v[20:23], v[52:55], v[44:47]
	v_mfma_i32_16x16x64_i8 v[48:51], v[28:31], v[52:55], v[48:51]
	v_mfma_i32_16x16x64_i8 v[52:55], v[16:19], v[56:59], v[148:151]
	v_mfma_i32_16x16x64_i8 v[56:59], v[24:27], v[56:59], v[144:147]
	v_mfma_i32_16x16x64_i8 v[52:55], v[20:23], v[60:63], v[52:55]
	v_mfma_i32_16x16x64_i8 v[56:59], v[28:31], v[60:63], v[56:59]
	s_barrier
	ds_read_b128 v[60:63], v221 offset:16384
	ds_read_b128 v[144:147], v221 offset:17408
	ds_read_b128 v[148:151], v221 offset:18432
	ds_read_b128 v[160:163], v221 offset:19456
	ds_read_b128 v[164:167], v221 offset:20480
	ds_read_b128 v[176:179], v221 offset:21504
	ds_read_b128 v[180:183], v221 offset:22528
	ds_read_b128 v[184:187], v221 offset:23552
	s_add_i32 m0, s59, 0x10000
	s_nop 0
	global_load_lds_dwordx4 v216, s[48:49]
	s_nop 0
	s_add_i32 m0, s59, 0x12000
	s_nop 0
	global_load_lds_dwordx4 v218, s[48:49]
	s_add_u32 s46, s48, 0x40000
	s_addc_u32 s47, s49, 0
	s_add_i32 m0, s59, 0x14000
	s_nop 0
	global_load_lds_dwordx4 v216, s[46:47]
	s_nop 0
	s_add_i32 m0, s59, 0x16000
	s_nop 0
	global_load_lds_dwordx4 v218, s[46:47]
	s_nop 0
	s_add_i32 m0, s59, 0
	s_nop 0
	global_load_lds_dwordx4 v215, s[52:53]
	s_nop 0
	s_add_i32 m0, s59, 0x2000
	s_nop 0
	global_load_lds_dwordx4 v217, s[52:53]
	s_waitcnt vmcnt(8) lgkmcnt(0)
	s_barrier
	v_mfma_i32_16x16x64_i8 v[140:143], v[0:3], v[60:63], v[140:143]
	v_mfma_i32_16x16x64_i8 v[124:127], v[0:3], v[148:151], v[124:127]
	v_mfma_i32_16x16x64_i8 v[108:111], v[0:3], v[164:167], v[108:111]
	v_mfma_i32_16x16x64_i8 v[0:3], v[0:3], v[180:183], v[88:91]
	v_mfma_i32_16x16x64_i8 v[136:139], v[8:11], v[60:63], v[136:139]
	v_mfma_i32_16x16x64_i8 v[120:123], v[8:11], v[148:151], v[120:123]
	v_mfma_i32_16x16x64_i8 v[104:107], v[8:11], v[164:167], v[104:107]
	v_mfma_i32_16x16x64_i8 v[88:91], v[4:7], v[184:187], v[0:3]
	v_mfma_i32_16x16x64_i8 v[0:3], v[8:11], v[180:183], v[84:87]
	v_mfma_i32_16x16x64_i8 v[140:143], v[4:7], v[144:147], v[140:143]
	v_mfma_i32_16x16x64_i8 v[136:139], v[12:15], v[144:147], v[136:139]
	v_mfma_i32_16x16x64_i8 v[124:127], v[4:7], v[160:163], v[124:127]
	v_mfma_i32_16x16x64_i8 v[120:123], v[12:15], v[160:163], v[120:123]
	v_mfma_i32_16x16x64_i8 v[108:111], v[4:7], v[176:179], v[108:111]
	v_mfma_i32_16x16x64_i8 v[104:107], v[12:15], v[176:179], v[104:107]
	v_mfma_i32_16x16x64_i8 v[84:87], v[12:15], v[184:187], v[0:3]
	v_mfma_i32_16x16x64_i8 v[0:3], v[16:19], v[60:63], v[132:135]
	v_mfma_i32_16x16x64_i8 v[132:135], v[20:23], v[144:147], v[0:3]
	v_mfma_i32_16x16x64_i8 v[0:3], v[24:27], v[60:63], v[128:131]
	v_mfma_i32_16x16x64_i8 v[128:131], v[28:31], v[144:147], v[0:3]
	v_mfma_i32_16x16x64_i8 v[0:3], v[16:19], v[148:151], v[116:119]
	v_mfma_i32_16x16x64_i8 v[116:119], v[20:23], v[160:163], v[0:3]
	v_mfma_i32_16x16x64_i8 v[0:3], v[24:27], v[148:151], v[112:115]
	v_mfma_i32_16x16x64_i8 v[112:115], v[28:31], v[160:163], v[0:3]
	v_mfma_i32_16x16x64_i8 v[0:3], v[16:19], v[164:167], v[100:103]
	v_mfma_i32_16x16x64_i8 v[100:103], v[20:23], v[176:179], v[0:3]
	v_mfma_i32_16x16x64_i8 v[0:3], v[24:27], v[164:167], v[96:99]
	v_mfma_i32_16x16x64_i8 v[96:99], v[28:31], v[176:179], v[0:3]
	v_mfma_i32_16x16x64_i8 v[0:3], v[16:19], v[180:183], v[72:75]
	v_mfma_i32_16x16x64_i8 v[72:75], v[20:23], v[184:187], v[0:3]
	v_mfma_i32_16x16x64_i8 v[0:3], v[24:27], v[180:183], v[68:71]
	v_mfma_i32_16x16x64_i8 v[68:71], v[28:31], v[184:187], v[0:3]
	s_barrier
	ds_read_b128 v[16:19], v222
	ds_read_b128 v[8:11], v222 offset:1024
	ds_read_b128 v[4:7], v222 offset:2048
	s_nop 1
	ds_read_b128 v[0:3], v222 offset:3072
	ds_read_b128 v[28:31], v223
	ds_read_b128 v[24:27], v223 offset:1024
	ds_read_b128 v[20:23], v223 offset:2048
	ds_read_b128 v[12:15], v223 offset:3072
	ds_read_b128 v[60:63], v221 offset:32768
	ds_read_b128 v[144:147], v221 offset:33792
	ds_read_b128 v[148:151], v221 offset:34816
	ds_read_b128 v[160:163], v221 offset:35840
	ds_read_b128 v[208:211], v221 offset:36864
	ds_read_b128 v[224:227], v221 offset:37888
	ds_read_b128 v[228:231], v221 offset:38912
	ds_read_b128 v[232:235], v221 offset:39936
	s_add_u32 s46, s52, 0x40000
	s_addc_u32 s47, s53, 0
	s_add_i32 m0, s59, 0x4000
	s_nop 0
	global_load_lds_dwordx4 v215, s[46:47]
	s_nop 0
	s_add_i32 m0, s59, 0x6000
	s_nop 0
	global_load_lds_dwordx4 v217, s[46:47]
	s_waitcnt vmcnt(8) lgkmcnt(0)
	s_barrier
	v_mfma_i32_16x16x64_i8 v[64:67], v[16:19], v[60:63], v[64:67]
	v_mfma_i32_16x16x64_i8 v[204:207], v[8:11], v[144:147], v[64:67]
	v_mfma_i32_16x16x64_i8 v[64:67], v[4:7], v[60:63], v[76:79]
	v_mfma_i32_16x16x64_i8 v[200:203], v[0:3], v[144:147], v[64:67]
	v_mfma_i32_16x16x64_i8 v[64:67], v[16:19], v[148:151], v[80:83]
	v_mfma_i32_16x16x64_i8 v[188:191], v[8:11], v[160:163], v[64:67]
	v_mfma_i32_16x16x64_i8 v[64:67], v[4:7], v[148:151], v[92:95]
	v_mfma_i32_16x16x64_i8 v[184:187], v[0:3], v[160:163], v[64:67]
	v_mfma_i32_16x16x64_i8 v[64:67], v[16:19], v[208:211], v[172:175]
	v_mfma_i32_16x16x64_i8 v[172:175], v[8:11], v[224:227], v[64:67]
	v_mfma_i32_16x16x64_i8 v[64:67], v[4:7], v[208:211], v[168:171]
	v_mfma_i32_16x16x64_i8 v[168:171], v[0:3], v[224:227], v[64:67]
	v_mfma_i32_16x16x64_i8 v[64:67], v[16:19], v[228:231], v[156:159]
	v_mfma_i32_16x16x64_i8 v[156:159], v[8:11], v[232:235], v[64:67]
	v_mfma_i32_16x16x64_i8 v[64:67], v[4:7], v[228:231], v[152:155]
	v_mfma_i32_16x16x64_i8 v[152:155], v[0:3], v[232:235], v[64:67]
	v_mfma_i32_16x16x64_i8 v[32:35], v[20:23], v[60:63], v[32:35]
	v_mfma_i32_16x16x64_i8 v[192:195], v[12:15], v[144:147], v[32:35]
	v_mfma_i32_16x16x64_i8 v[32:35], v[28:31], v[148:151], v[36:39]
	v_mfma_i32_16x16x64_i8 v[180:183], v[24:27], v[160:163], v[32:35]
	v_mfma_i32_16x16x64_i8 v[32:35], v[20:23], v[148:151], v[40:43]
	v_mfma_i32_16x16x64_i8 v[176:179], v[12:15], v[160:163], v[32:35]
	v_mfma_i32_16x16x64_i8 v[32:35], v[28:31], v[208:211], v[44:47]
	v_mfma_i32_16x16x64_i8 v[164:167], v[24:27], v[224:227], v[32:35]
	v_mfma_i32_16x16x64_i8 v[32:35], v[20:23], v[208:211], v[48:51]
	v_mfma_i32_16x16x64_i8 v[160:163], v[12:15], v[224:227], v[32:35]
	v_mfma_i32_16x16x64_i8 v[32:35], v[28:31], v[228:231], v[52:55]
	v_mfma_i32_16x16x64_i8 v[64:67], v[28:31], v[60:63], v[196:199]
	v_mfma_i32_16x16x64_i8 v[148:151], v[24:27], v[232:235], v[32:35]
	v_mfma_i32_16x16x64_i8 v[32:35], v[20:23], v[228:231], v[56:59]
	v_mfma_i32_16x16x64_i8 v[196:199], v[24:27], v[144:147], v[64:67]
	v_mfma_i32_16x16x64_i8 v[144:147], v[12:15], v[232:235], v[32:35]
	s_barrier
	ds_read_b128 v[60:63], v221 offset:49152
	ds_read_b128 v[56:59], v221 offset:50176
	ds_read_b128 v[52:55], v221 offset:51200
	ds_read_b128 v[48:51], v221 offset:52224
	ds_read_b128 v[44:47], v221 offset:53248
	ds_read_b128 v[40:43], v221 offset:54272
	ds_read_b128 v[36:39], v221 offset:55296
	ds_read_b128 v[32:35], v221 offset:56320
	s_add_i32 m0, s59, 0x18000
	s_nop 0
	global_load_lds_dwordx4 v216, s[50:51]
	s_nop 0
	s_add_i32 m0, s59, 0x1a000
	s_nop 0
	global_load_lds_dwordx4 v218, s[50:51]
	s_add_u32 s46, s48, 0x40080
	s_addc_u32 s47, s49, 0
	s_add_i32 m0, s59, 0x1c000
	s_nop 0
	global_load_lds_dwordx4 v216, s[46:47]
	s_nop 0
	s_add_i32 m0, s59, 0x1e000
	s_nop 0
	global_load_lds_dwordx4 v218, s[46:47]
	s_nop 0
	s_add_i32 m0, s59, 0x8000
	s_nop 0
	global_load_lds_dwordx4 v215, s[12:13]
	s_nop 0
	s_add_i32 m0, s59, 0xa000
	s_nop 0
	global_load_lds_dwordx4 v217, s[12:13]
	s_add_i32 s76, s76, 2
	s_add_u32 s77, s77, 0x100
	s_addc_u32 s80, s80, 0
	s_cmp_gt_u32 s76, 13
	s_mov_b64 s[46:47], s[8:9]
	s_waitcnt vmcnt(8) lgkmcnt(0)
	s_barrier
	v_mfma_i32_16x16x64_i8 v[64:67], v[16:19], v[60:63], v[140:143]
	v_mfma_i32_16x16x64_i8 v[140:143], v[8:11], v[56:59], v[64:67]
	v_mfma_i32_16x16x64_i8 v[64:67], v[4:7], v[60:63], v[136:139]
	v_mfma_i32_16x16x64_i8 v[136:139], v[0:3], v[56:59], v[64:67]
	v_mfma_i32_16x16x64_i8 v[64:67], v[16:19], v[52:55], v[124:127]
	v_mfma_i32_16x16x64_i8 v[124:127], v[8:11], v[48:51], v[64:67]
	v_mfma_i32_16x16x64_i8 v[64:67], v[4:7], v[52:55], v[120:123]
	v_mfma_i32_16x16x64_i8 v[120:123], v[0:3], v[48:51], v[64:67]
	v_mfma_i32_16x16x64_i8 v[64:67], v[16:19], v[44:47], v[108:111]
	v_mfma_i32_16x16x64_i8 v[108:111], v[8:11], v[40:43], v[64:67]
	v_mfma_i32_16x16x64_i8 v[64:67], v[4:7], v[44:47], v[104:107]
	v_mfma_i32_16x16x64_i8 v[104:107], v[0:3], v[40:43], v[64:67]
	v_mfma_i32_16x16x64_i8 v[64:67], v[16:19], v[36:39], v[88:91]
	v_mfma_i32_16x16x64_i8 v[88:91], v[8:11], v[32:35], v[64:67]
	v_mfma_i32_16x16x64_i8 v[64:67], v[4:7], v[36:39], v[84:87]
	v_mfma_i32_16x16x64_i8 v[84:87], v[0:3], v[32:35], v[64:67]
	v_mfma_i32_16x16x64_i8 v[64:67], v[28:31], v[60:63], v[132:135]
	v_mfma_i32_16x16x64_i8 v[132:135], v[24:27], v[56:59], v[64:67]
	v_mfma_i32_16x16x64_i8 v[64:67], v[20:23], v[60:63], v[128:131]
	v_mfma_i32_16x16x64_i8 v[128:131], v[12:15], v[56:59], v[64:67]
	v_mfma_i32_16x16x64_i8 v[64:67], v[28:31], v[52:55], v[116:119]
	v_mfma_i32_16x16x64_i8 v[116:119], v[24:27], v[48:51], v[64:67]
	v_mfma_i32_16x16x64_i8 v[64:67], v[20:23], v[52:55], v[112:115]
	v_mfma_i32_16x16x64_i8 v[112:115], v[12:15], v[48:51], v[64:67]
	v_mfma_i32_16x16x64_i8 v[64:67], v[28:31], v[44:47], v[100:103]
	v_mfma_i32_16x16x64_i8 v[100:103], v[24:27], v[40:43], v[64:67]
	v_mfma_i32_16x16x64_i8 v[64:67], v[20:23], v[44:47], v[96:99]
	v_mfma_i32_16x16x64_i8 v[96:99], v[12:15], v[40:43], v[64:67]
	v_mfma_i32_16x16x64_i8 v[64:67], v[28:31], v[36:39], v[72:75]
	v_mfma_i32_16x16x64_i8 v[72:75], v[24:27], v[32:35], v[64:67]
	v_mfma_i32_16x16x64_i8 v[64:67], v[20:23], v[36:39], v[68:71]
	v_mfma_i32_16x16x64_i8 v[68:71], v[12:15], v[32:35], v[64:67]
	s_barrier
	s_cbranch_scc0 .LBB0_261
	s_and_b64 vcc, exec, s[28:29]
	s_cbranch_vccz .LBB0_264
	s_barrier

.LBB0_603:
	ds_read_b128 v[100:103], v217
	ds_read_b128 v[108:111], v217 offset:1024
	ds_read_b128 v[116:119], v217 offset:2048
	ds_read_b128 v[124:127], v217 offset:3072
	ds_read_b128 v[132:135], v218
	ds_read_b128 v[140:143], v218 offset:1024
	ds_read_b128 v[148:151], v218 offset:2048
	ds_read_b128 v[156:159], v218 offset:3072
	ds_read_b128 v[160:163], v219
	ds_read_b128 v[164:167], v219 offset:1024
	ds_read_b128 v[168:171], v219 offset:2048
	ds_read_b128 v[172:175], v219 offset:3072
	ds_read_b128 v[176:179], v219 offset:4096
	ds_read_b128 v[180:183], v219 offset:5120
	ds_read_b128 v[184:187], v219 offset:6144
	ds_read_b128 v[194:197], v219 offset:7168
	s_add_u32 s30, s36, 0x100
	s_addc_u32 s31, s37, 0
	s_cmp_eq_u32 s61, 28
	s_cselect_b32 s42, s9, s30
	s_cselect_b32 s43, s7, s31
	s_cselect_b32 s38, s25, s59
	s_cselect_b32 s39, s23, s60
	s_add_u32 s34, s42, 0x80
	s_addc_u32 s35, s43, 0
	s_add_u32 s40, s38, 0x80
	s_addc_u32 s41, s39, 0
	s_add_u32 s36, s36, 0x80080
	s_addc_u32 s37, s37, 0
	s_add_i32 m0, s48, 0xc000
	s_nop 0
	global_load_lds_dwordx4 v213, s[36:37]
	s_nop 0
	s_add_i32 m0, s48, 0xe000
	s_nop 0
	global_load_lds_dwordx4 v214, s[36:37]
	s_waitcnt vmcnt(8) lgkmcnt(0)
	s_barrier
	v_mfma_f32_16x16x32_bf16 v[152:155], v[100:103], v[160:163], v[152:155]
	v_mfma_f32_16x16x32_bf16 v[144:147], v[116:119], v[160:163], v[144:147]
	v_mfma_f32_16x16x32_bf16 v[112:115], v[116:119], v[168:171], v[112:115]
	v_mfma_f32_16x16x32_bf16 v[120:123], v[100:103], v[168:171], v[120:123]
	v_mfma_f32_16x16x32_bf16 v[92:95], v[100:103], v[176:179], v[92:95]
	v_mfma_f32_16x16x32_bf16 v[88:91], v[116:119], v[176:179], v[88:91]
	v_mfma_f32_16x16x32_bf16 v[72:75], v[116:119], v[184:187], v[72:75]
	v_mfma_f32_16x16x32_bf16 v[76:79], v[100:103], v[184:187], v[76:79]
	v_mfma_f32_16x16x32_bf16 v[152:155], v[108:111], v[164:167], v[152:155]
	v_mfma_f32_16x16x32_bf16 v[144:147], v[124:127], v[164:167], v[144:147]
	v_mfma_f32_16x16x32_bf16 v[112:115], v[124:127], v[172:175], v[112:115]
	v_mfma_f32_16x16x32_bf16 v[120:123], v[108:111], v[172:175], v[120:123]
	v_mfma_f32_16x16x32_bf16 v[92:95], v[108:111], v[180:183], v[92:95]
	v_mfma_f32_16x16x32_bf16 v[88:91], v[124:127], v[180:183], v[88:91]
	v_mfma_f32_16x16x32_bf16 v[72:75], v[124:127], v[194:197], v[72:75]
	v_mfma_f32_16x16x32_bf16 v[76:79], v[108:111], v[194:197], v[76:79]
	v_mfma_f32_16x16x32_bf16 v[136:139], v[132:135], v[160:163], v[136:139]
	v_mfma_f32_16x16x32_bf16 v[128:131], v[148:151], v[160:163], v[128:131]
	v_mfma_f32_16x16x32_bf16 v[96:99], v[148:151], v[168:171], v[96:99]
	v_mfma_f32_16x16x32_bf16 v[104:107], v[132:135], v[168:171], v[104:107]
	v_mfma_f32_16x16x32_bf16 v[84:87], v[132:135], v[176:179], v[84:87]
	v_mfma_f32_16x16x32_bf16 v[80:83], v[148:151], v[176:179], v[80:83]
	v_mfma_f32_16x16x32_bf16 v[64:67], v[148:151], v[184:187], v[64:67]
	v_mfma_f32_16x16x32_bf16 v[68:71], v[132:135], v[184:187], v[68:71]
	v_mfma_f32_16x16x32_bf16 v[136:139], v[140:143], v[164:167], v[136:139]
	v_mfma_f32_16x16x32_bf16 v[128:131], v[156:159], v[164:167], v[128:131]
	v_mfma_f32_16x16x32_bf16 v[96:99], v[156:159], v[172:175], v[96:99]
	v_mfma_f32_16x16x32_bf16 v[104:107], v[140:143], v[172:175], v[104:107]
	v_mfma_f32_16x16x32_bf16 v[84:87], v[140:143], v[180:183], v[84:87]
	v_mfma_f32_16x16x32_bf16 v[80:83], v[156:159], v[180:183], v[80:83]
	v_mfma_f32_16x16x32_bf16 v[64:67], v[156:159], v[194:197], v[64:67]
	v_mfma_f32_16x16x32_bf16 v[68:71], v[140:143], v[194:197], v[68:71]
	s_barrier
	ds_read_b128 v[160:163], v219 offset:16384
	ds_read_b128 v[164:167], v219 offset:17408
	ds_read_b128 v[168:171], v219 offset:18432
	ds_read_b128 v[172:175], v219 offset:19456
	ds_read_b128 v[176:179], v219 offset:20480
	ds_read_b128 v[180:183], v219 offset:21504
	ds_read_b128 v[184:187], v219 offset:22528
	ds_read_b128 v[194:197], v219 offset:23552
	s_add_i32 m0, s48, 0x10000
	s_nop 0
	global_load_lds_dwordx4 v213, s[38:39]
	s_nop 0
	s_add_i32 m0, s48, 0x12000
	s_nop 0
	global_load_lds_dwordx4 v214, s[38:39]
	s_add_u32 s36, s38, 0x80000
	s_addc_u32 s37, s39, 0
	s_add_i32 m0, s48, 0x14000
	s_nop 0
	global_load_lds_dwordx4 v213, s[36:37]
	s_nop 0
	s_add_i32 m0, s48, 0x16000
	s_nop 0
	global_load_lds_dwordx4 v214, s[36:37]
	s_nop 0
	s_add_i32 m0, s48, 0
	s_nop 0
	global_load_lds_dwordx4 v213, s[42:43]
	s_nop 0
	s_add_i32 m0, s48, 0x2000
	s_nop 0
	global_load_lds_dwordx4 v214, s[42:43]
	s_waitcnt vmcnt(8) lgkmcnt(0)
	s_barrier
	v_mfma_f32_16x16x32_bf16 v[60:63], v[100:103], v[160:163], v[60:63]
	v_mfma_f32_16x16x32_bf16 v[56:59], v[116:119], v[160:163], v[56:59]
	v_mfma_f32_16x16x32_bf16 v[40:43], v[116:119], v[168:171], v[40:43]
	v_mfma_f32_16x16x32_bf16 v[44:47], v[100:103], v[168:171], v[44:47]
	v_mfma_f32_16x16x32_bf16 v[28:31], v[100:103], v[176:179], v[28:31]
	v_mfma_f32_16x16x32_bf16 v[24:27], v[116:119], v[176:179], v[24:27]
	v_mfma_f32_16x16x32_bf16 v[8:11], v[116:119], v[184:187], v[8:11]
	v_mfma_f32_16x16x32_bf16 v[12:15], v[100:103], v[184:187], v[12:15]
	v_mfma_f32_16x16x32_bf16 v[60:63], v[108:111], v[164:167], v[60:63]
	v_mfma_f32_16x16x32_bf16 v[56:59], v[124:127], v[164:167], v[56:59]
	v_mfma_f32_16x16x32_bf16 v[40:43], v[124:127], v[172:175], v[40:43]
	v_mfma_f32_16x16x32_bf16 v[44:47], v[108:111], v[172:175], v[44:47]
	v_mfma_f32_16x16x32_bf16 v[28:31], v[108:111], v[180:183], v[28:31]
	v_mfma_f32_16x16x32_bf16 v[24:27], v[124:127], v[180:183], v[24:27]
	v_mfma_f32_16x16x32_bf16 v[8:11], v[124:127], v[194:197], v[8:11]
	v_mfma_f32_16x16x32_bf16 v[12:15], v[108:111], v[194:197], v[12:15]
	v_mfma_f32_16x16x32_bf16 v[52:55], v[132:135], v[160:163], v[52:55]
	v_mfma_f32_16x16x32_bf16 v[48:51], v[148:151], v[160:163], v[48:51]
	v_mfma_f32_16x16x32_bf16 v[32:35], v[148:151], v[168:171], v[32:35]
	v_mfma_f32_16x16x32_bf16 v[36:39], v[132:135], v[168:171], v[36:39]
	v_mfma_f32_16x16x32_bf16 v[20:23], v[132:135], v[176:179], v[20:23]
	v_mfma_f32_16x16x32_bf16 v[16:19], v[148:151], v[176:179], v[16:19]
	v_mfma_f32_16x16x32_bf16 v[0:3], v[148:151], v[184:187], v[0:3]
	v_mfma_f32_16x16x32_bf16 v[4:7], v[132:135], v[184:187], v[4:7]
	v_mfma_f32_16x16x32_bf16 v[52:55], v[140:143], v[164:167], v[52:55]
	v_mfma_f32_16x16x32_bf16 v[48:51], v[156:159], v[164:167], v[48:51]
	v_mfma_f32_16x16x32_bf16 v[32:35], v[156:159], v[172:175], v[32:35]
	v_mfma_f32_16x16x32_bf16 v[36:39], v[140:143], v[172:175], v[36:39]
	v_mfma_f32_16x16x32_bf16 v[20:23], v[140:143], v[180:183], v[20:23]
	v_mfma_f32_16x16x32_bf16 v[16:19], v[156:159], v[180:183], v[16:19]
	v_mfma_f32_16x16x32_bf16 v[0:3], v[156:159], v[194:197], v[0:3]
	v_mfma_f32_16x16x32_bf16 v[4:7], v[140:143], v[194:197], v[4:7]
	s_barrier
	ds_read_b128 v[100:103], v220
	ds_read_b128 v[108:111], v220 offset:1024
	ds_read_b128 v[116:119], v220 offset:2048
	ds_read_b128 v[124:127], v220 offset:3072
	ds_read_b128 v[132:135], v221
	ds_read_b128 v[140:143], v221 offset:1024
	ds_read_b128 v[148:151], v221 offset:2048
	ds_read_b128 v[156:159], v221 offset:3072
	ds_read_b128 v[160:163], v219 offset:32768
	ds_read_b128 v[164:167], v219 offset:33792
	ds_read_b128 v[168:171], v219 offset:34816
	ds_read_b128 v[172:175], v219 offset:35840
	ds_read_b128 v[176:179], v219 offset:36864
	ds_read_b128 v[180:183], v219 offset:37888
	ds_read_b128 v[184:187], v219 offset:38912
	ds_read_b128 v[194:197], v219 offset:39936
	s_add_u32 s36, s42, 0x80000
	s_addc_u32 s37, s43, 0
	s_add_i32 m0, s48, 0x4000
	s_nop 0
	global_load_lds_dwordx4 v213, s[36:37]
	s_nop 0
	s_add_i32 m0, s48, 0x6000
	s_nop 0
	global_load_lds_dwordx4 v214, s[36:37]
	s_waitcnt vmcnt(8) lgkmcnt(0)
	s_barrier
	v_mfma_f32_16x16x32_bf16 v[152:155], v[100:103], v[160:163], v[152:155]
	v_mfma_f32_16x16x32_bf16 v[144:147], v[116:119], v[160:163], v[144:147]
	v_mfma_f32_16x16x32_bf16 v[112:115], v[116:119], v[168:171], v[112:115]
	v_mfma_f32_16x16x32_bf16 v[120:123], v[100:103], v[168:171], v[120:123]
	v_mfma_f32_16x16x32_bf16 v[92:95], v[100:103], v[176:179], v[92:95]
	v_mfma_f32_16x16x32_bf16 v[88:91], v[116:119], v[176:179], v[88:91]
	v_mfma_f32_16x16x32_bf16 v[72:75], v[116:119], v[184:187], v[72:75]
	v_mfma_f32_16x16x32_bf16 v[76:79], v[100:103], v[184:187], v[76:79]
	v_mfma_f32_16x16x32_bf16 v[152:155], v[108:111], v[164:167], v[152:155]
	v_mfma_f32_16x16x32_bf16 v[144:147], v[124:127], v[164:167], v[144:147]
	v_mfma_f32_16x16x32_bf16 v[112:115], v[124:127], v[172:175], v[112:115]
	v_mfma_f32_16x16x32_bf16 v[120:123], v[108:111], v[172:175], v[120:123]
	v_mfma_f32_16x16x32_bf16 v[92:95], v[108:111], v[180:183], v[92:95]
	v_mfma_f32_16x16x32_bf16 v[88:91], v[124:127], v[180:183], v[88:91]
	v_mfma_f32_16x16x32_bf16 v[72:75], v[124:127], v[194:197], v[72:75]
	v_mfma_f32_16x16x32_bf16 v[76:79], v[108:111], v[194:197], v[76:79]
	v_mfma_f32_16x16x32_bf16 v[136:139], v[132:135], v[160:163], v[136:139]
	v_mfma_f32_16x16x32_bf16 v[128:131], v[148:151], v[160:163], v[128:131]
	v_mfma_f32_16x16x32_bf16 v[96:99], v[148:151], v[168:171], v[96:99]
	v_mfma_f32_16x16x32_bf16 v[104:107], v[132:135], v[168:171], v[104:107]
	v_mfma_f32_16x16x32_bf16 v[84:87], v[132:135], v[176:179], v[84:87]
	v_mfma_f32_16x16x32_bf16 v[80:83], v[148:151], v[176:179], v[80:83]
	v_mfma_f32_16x16x32_bf16 v[64:67], v[148:151], v[184:187], v[64:67]
	v_mfma_f32_16x16x32_bf16 v[68:71], v[132:135], v[184:187], v[68:71]
	v_mfma_f32_16x16x32_bf16 v[136:139], v[140:143], v[164:167], v[136:139]
	v_mfma_f32_16x16x32_bf16 v[128:131], v[156:159], v[164:167], v[128:131]
	v_mfma_f32_16x16x32_bf16 v[96:99], v[156:159], v[172:175], v[96:99]
	v_mfma_f32_16x16x32_bf16 v[104:107], v[140:143], v[172:175], v[104:107]
	v_mfma_f32_16x16x32_bf16 v[84:87], v[140:143], v[180:183], v[84:87]
	v_mfma_f32_16x16x32_bf16 v[80:83], v[156:159], v[180:183], v[80:83]
	v_mfma_f32_16x16x32_bf16 v[64:67], v[156:159], v[194:197], v[64:67]
	v_mfma_f32_16x16x32_bf16 v[68:71], v[140:143], v[194:197], v[68:71]
	s_barrier
	ds_read_b128 v[160:163], v219 offset:49152
	ds_read_b128 v[164:167], v219 offset:50176
	ds_read_b128 v[168:171], v219 offset:51200
	ds_read_b128 v[172:175], v219 offset:52224
	ds_read_b128 v[176:179], v219 offset:53248
	ds_read_b128 v[180:183], v219 offset:54272
	ds_read_b128 v[184:187], v219 offset:55296
	ds_read_b128 v[194:197], v219 offset:56320
	s_add_i32 m0, s48, 0x18000
	s_nop 0
	global_load_lds_dwordx4 v213, s[40:41]
	s_nop 0
	s_add_i32 m0, s48, 0x1a000
	s_nop 0
	global_load_lds_dwordx4 v214, s[40:41]
	s_add_u32 s36, s38, 0x80080
	s_addc_u32 s37, s39, 0
	s_add_i32 m0, s48, 0x1c000
	s_nop 0
	global_load_lds_dwordx4 v213, s[36:37]
	s_nop 0
	s_add_i32 m0, s48, 0x1e000
	s_nop 0
	global_load_lds_dwordx4 v214, s[36:37]
	s_nop 0
	s_add_i32 m0, s48, 0x8000
	s_nop 0
	global_load_lds_dwordx4 v213, s[34:35]
	s_nop 0
	s_add_i32 m0, s48, 0xa000
	s_nop 0
	global_load_lds_dwordx4 v214, s[34:35]
	s_add_i32 s61, s61, 2
	s_add_u32 s59, s59, 0x100
	s_addc_u32 s60, s60, 0
	s_cmp_gt_u32 s61, 29
	s_mov_b64 s[36:37], s[30:31]
	s_waitcnt vmcnt(8) lgkmcnt(0)
	s_barrier
	v_mfma_f32_16x16x32_bf16 v[60:63], v[100:103], v[160:163], v[60:63]
	v_mfma_f32_16x16x32_bf16 v[56:59], v[116:119], v[160:163], v[56:59]
	v_mfma_f32_16x16x32_bf16 v[40:43], v[116:119], v[168:171], v[40:43]
	v_mfma_f32_16x16x32_bf16 v[44:47], v[100:103], v[168:171], v[44:47]
	v_mfma_f32_16x16x32_bf16 v[28:31], v[100:103], v[176:179], v[28:31]
	v_mfma_f32_16x16x32_bf16 v[24:27], v[116:119], v[176:179], v[24:27]
	v_mfma_f32_16x16x32_bf16 v[8:11], v[116:119], v[184:187], v[8:11]
	v_mfma_f32_16x16x32_bf16 v[12:15], v[100:103], v[184:187], v[12:15]
	v_mfma_f32_16x16x32_bf16 v[60:63], v[108:111], v[164:167], v[60:63]
	v_mfma_f32_16x16x32_bf16 v[56:59], v[124:127], v[164:167], v[56:59]
	v_mfma_f32_16x16x32_bf16 v[40:43], v[124:127], v[172:175], v[40:43]
	v_mfma_f32_16x16x32_bf16 v[44:47], v[108:111], v[172:175], v[44:47]
	v_mfma_f32_16x16x32_bf16 v[28:31], v[108:111], v[180:183], v[28:31]
	v_mfma_f32_16x16x32_bf16 v[24:27], v[124:127], v[180:183], v[24:27]
	v_mfma_f32_16x16x32_bf16 v[8:11], v[124:127], v[194:197], v[8:11]
	v_mfma_f32_16x16x32_bf16 v[12:15], v[108:111], v[194:197], v[12:15]
	v_mfma_f32_16x16x32_bf16 v[52:55], v[132:135], v[160:163], v[52:55]
	v_mfma_f32_16x16x32_bf16 v[48:51], v[148:151], v[160:163], v[48:51]
	v_mfma_f32_16x16x32_bf16 v[32:35], v[148:151], v[168:171], v[32:35]
	v_mfma_f32_16x16x32_bf16 v[36:39], v[132:135], v[168:171], v[36:39]
	v_mfma_f32_16x16x32_bf16 v[20:23], v[132:135], v[176:179], v[20:23]
	v_mfma_f32_16x16x32_bf16 v[16:19], v[148:151], v[176:179], v[16:19]
	v_mfma_f32_16x16x32_bf16 v[0:3], v[148:151], v[184:187], v[0:3]
	v_mfma_f32_16x16x32_bf16 v[4:7], v[132:135], v[184:187], v[4:7]
	v_mfma_f32_16x16x32_bf16 v[52:55], v[140:143], v[164:167], v[52:55]
	v_mfma_f32_16x16x32_bf16 v[48:51], v[156:159], v[164:167], v[48:51]
	v_mfma_f32_16x16x32_bf16 v[32:35], v[156:159], v[172:175], v[32:35]
	v_mfma_f32_16x16x32_bf16 v[36:39], v[140:143], v[172:175], v[36:39]
	v_mfma_f32_16x16x32_bf16 v[20:23], v[140:143], v[180:183], v[20:23]
	v_mfma_f32_16x16x32_bf16 v[16:19], v[156:159], v[180:183], v[16:19]
	v_mfma_f32_16x16x32_bf16 v[0:3], v[156:159], v[194:197], v[0:3]
	v_mfma_f32_16x16x32_bf16 v[4:7], v[140:143], v[194:197], v[4:7]
	s_barrier
	s_cbranch_scc0 .LBB0_603
	s_and_b64 vcc, exec, s[20:21]
	s_cbranch_vccz .LBB0_606
	s_barrier

.LBB0_755:
	ds_read_b128 v[20:23], v205
	ds_read_b128 v[24:27], v205 offset:1024
	ds_read_b128 v[28:31], v205 offset:2048
	ds_read_b128 v[32:35], v205 offset:3072
	ds_read_b128 v[36:39], v204
	ds_read_b128 v[40:43], v204 offset:1024
	ds_read_b128 v[52:55], v204 offset:2048
	ds_read_b128 v[56:59], v204 offset:3072
	ds_read_b128 v[64:67], v206
	ds_read_b128 v[68:71], v206 offset:1024
	ds_read_b128 v[72:75], v206 offset:2048
	ds_read_b128 v[76:79], v206 offset:3072
	ds_read_b128 v[80:83], v206 offset:4096
	ds_read_b128 v[84:87], v206 offset:5120
	ds_read_b128 v[88:91], v206 offset:6144
	ds_read_b128 v[92:95], v206 offset:7168
	s_add_u32 s24, s26, 0x100
	s_addc_u32 s25, s27, 0
	s_and_b64 s[30:31], s[30:31], exec
	s_cselect_b32 s38, s59, s24
	s_cselect_b32 s39, s58, s25
	s_cselect_b32 s35, s15, s62
	s_cselect_b32 s34, s60, s61
	s_add_u32 s30, s38, 0x80
	s_addc_u32 s31, s39, 0
	s_add_u32 s36, s34, 0x80
	s_addc_u32 s37, s35, 0
	s_add_u32 s26, s26, 0x40080
	s_addc_u32 s27, s27, 0
	s_add_i32 m0, s46, 0xc000
	s_nop 0
	global_load_lds_dwordx4 v199, s[26:27]
	s_nop 0
	s_add_i32 m0, s46, 0xe000
	s_nop 0
	global_load_lds_dwordx4 v201, s[26:27]
	s_waitcnt vmcnt(8) lgkmcnt(0)
	s_barrier
	v_mfma_i32_16x16x64_i8 v[184:187], v[20:23], v[64:67], v[184:187]
	v_mfma_i32_16x16x64_i8 v[176:179], v[28:31], v[64:67], v[176:179]
	v_mfma_i32_16x16x64_i8 v[160:163], v[28:31], v[72:75], v[160:163]
	v_mfma_i32_16x16x64_i8 v[168:171], v[20:23], v[72:75], v[168:171]
	v_mfma_i32_16x16x64_i8 v[152:155], v[20:23], v[80:83], v[152:155]
	v_mfma_i32_16x16x64_i8 v[144:147], v[28:31], v[80:83], v[144:147]
	v_mfma_i32_16x16x64_i8 v[128:131], v[28:31], v[88:91], v[128:131]
	v_mfma_i32_16x16x64_i8 v[136:139], v[20:23], v[88:91], v[136:139]
	v_mfma_i32_16x16x64_i8 v[184:187], v[24:27], v[68:71], v[184:187]
	v_mfma_i32_16x16x64_i8 v[176:179], v[32:35], v[68:71], v[176:179]
	v_mfma_i32_16x16x64_i8 v[160:163], v[32:35], v[76:79], v[160:163]
	v_mfma_i32_16x16x64_i8 v[168:171], v[24:27], v[76:79], v[168:171]
	v_mfma_i32_16x16x64_i8 v[152:155], v[24:27], v[84:87], v[152:155]
	v_mfma_i32_16x16x64_i8 v[144:147], v[32:35], v[84:87], v[144:147]
	v_mfma_i32_16x16x64_i8 v[128:131], v[32:35], v[92:95], v[128:131]
	v_mfma_i32_16x16x64_i8 v[136:139], v[24:27], v[92:95], v[136:139]
	v_mfma_i32_16x16x64_i8 v[188:191], v[36:39], v[64:67], v[188:191]
	v_mfma_i32_16x16x64_i8 v[64:67], v[52:55], v[64:67], v[180:183]
	v_mfma_i32_16x16x64_i8 v[188:191], v[40:43], v[68:71], v[188:191]
	v_mfma_i32_16x16x64_i8 v[64:67], v[56:59], v[68:71], v[64:67]
	v_mfma_i32_16x16x64_i8 v[68:71], v[36:39], v[72:75], v[172:175]
	v_mfma_i32_16x16x64_i8 v[72:75], v[52:55], v[72:75], v[164:167]
	v_mfma_i32_16x16x64_i8 v[68:71], v[40:43], v[76:79], v[68:71]
	v_mfma_i32_16x16x64_i8 v[72:75], v[56:59], v[76:79], v[72:75]
	v_mfma_i32_16x16x64_i8 v[76:79], v[36:39], v[80:83], v[156:159]
	v_mfma_i32_16x16x64_i8 v[80:83], v[52:55], v[80:83], v[148:151]
	v_mfma_i32_16x16x64_i8 v[76:79], v[40:43], v[84:87], v[76:79]
	v_mfma_i32_16x16x64_i8 v[80:83], v[56:59], v[84:87], v[80:83]
	v_mfma_i32_16x16x64_i8 v[84:87], v[36:39], v[88:91], v[140:143]
	v_mfma_i32_16x16x64_i8 v[88:91], v[52:55], v[88:91], v[132:135]
	v_mfma_i32_16x16x64_i8 v[84:87], v[40:43], v[92:95], v[84:87]
	v_mfma_i32_16x16x64_i8 v[88:91], v[56:59], v[92:95], v[88:91]
	s_barrier
	ds_read_b128 v[92:95], v206 offset:16384
	ds_read_b128 v[132:135], v206 offset:17408
	ds_read_b128 v[140:143], v206 offset:18432
	ds_read_b128 v[148:151], v206 offset:19456
	ds_read_b128 v[156:159], v206 offset:20480
	ds_read_b128 v[164:167], v206 offset:21504
	ds_read_b128 v[172:175], v206 offset:22528
	ds_read_b128 v[180:183], v206 offset:23552
	s_add_i32 m0, s46, 0x10000
	s_nop 0
	global_load_lds_dwordx4 v200, s[34:35]
	s_nop 0
	s_add_i32 m0, s46, 0x12000
	s_nop 0
	global_load_lds_dwordx4 v202, s[34:35]
	s_add_u32 s26, s34, 0x40000
	s_addc_u32 s27, s35, 0
	s_add_i32 m0, s46, 0x14000
	s_nop 0
	global_load_lds_dwordx4 v200, s[26:27]
	s_nop 0
	s_add_i32 m0, s46, 0x16000
	s_nop 0
	global_load_lds_dwordx4 v202, s[26:27]
	s_nop 0
	s_add_i32 m0, s46, 0
	s_nop 0
	global_load_lds_dwordx4 v199, s[38:39]
	s_nop 0
	s_add_i32 m0, s46, 0x2000
	s_nop 0
	global_load_lds_dwordx4 v201, s[38:39]
	s_waitcnt vmcnt(8) lgkmcnt(0)
	s_barrier
	v_mfma_i32_16x16x64_i8 v[120:123], v[20:23], v[92:95], v[120:123]
	v_mfma_i32_16x16x64_i8 v[112:115], v[28:31], v[92:95], v[112:115]
	v_mfma_i32_16x16x64_i8 v[96:99], v[28:31], v[140:143], v[96:99]
	v_mfma_i32_16x16x64_i8 v[104:107], v[20:23], v[140:143], v[104:107]
	v_mfma_i32_16x16x64_i8 v[48:51], v[20:23], v[156:159], v[48:51]
	v_mfma_i32_16x16x64_i8 v[16:19], v[28:31], v[156:159], v[16:19]
	v_mfma_i32_16x16x64_i8 v[0:3], v[28:31], v[172:175], v[0:3]
	v_mfma_i32_16x16x64_i8 v[8:11], v[20:23], v[172:175], v[8:11]
	v_mfma_i32_16x16x64_i8 v[120:123], v[24:27], v[132:135], v[120:123]
	v_mfma_i32_16x16x64_i8 v[112:115], v[32:35], v[132:135], v[112:115]
	v_mfma_i32_16x16x64_i8 v[96:99], v[32:35], v[148:151], v[96:99]
	v_mfma_i32_16x16x64_i8 v[104:107], v[24:27], v[148:151], v[104:107]
	v_mfma_i32_16x16x64_i8 v[48:51], v[24:27], v[164:167], v[48:51]
	v_mfma_i32_16x16x64_i8 v[16:19], v[32:35], v[164:167], v[16:19]
	v_mfma_i32_16x16x64_i8 v[0:3], v[32:35], v[180:183], v[0:3]
	v_mfma_i32_16x16x64_i8 v[8:11], v[24:27], v[180:183], v[8:11]
	v_mfma_i32_16x16x64_i8 v[20:23], v[36:39], v[92:95], v[124:127]
	v_mfma_i32_16x16x64_i8 v[124:127], v[40:43], v[132:135], v[20:23]
	v_mfma_i32_16x16x64_i8 v[20:23], v[52:55], v[92:95], v[116:119]
	v_mfma_i32_16x16x64_i8 v[116:119], v[56:59], v[132:135], v[20:23]
	v_mfma_i32_16x16x64_i8 v[20:23], v[36:39], v[140:143], v[108:111]
	v_mfma_i32_16x16x64_i8 v[108:111], v[40:43], v[148:151], v[20:23]
	v_mfma_i32_16x16x64_i8 v[20:23], v[52:55], v[140:143], v[100:103]
	v_mfma_i32_16x16x64_i8 v[100:103], v[56:59], v[148:151], v[20:23]
	v_mfma_i32_16x16x64_i8 v[20:23], v[36:39], v[156:159], v[60:63]
	v_mfma_i32_16x16x64_i8 v[60:63], v[40:43], v[164:167], v[20:23]
	v_mfma_i32_16x16x64_i8 v[20:23], v[52:55], v[156:159], v[44:47]
	v_mfma_i32_16x16x64_i8 v[12:15], v[36:39], v[172:175], v[12:15]
	v_mfma_i32_16x16x64_i8 v[4:7], v[52:55], v[172:175], v[4:7]
	v_mfma_i32_16x16x64_i8 v[44:47], v[56:59], v[164:167], v[20:23]
	v_mfma_i32_16x16x64_i8 v[12:15], v[40:43], v[180:183], v[12:15]
	v_mfma_i32_16x16x64_i8 v[4:7], v[56:59], v[180:183], v[4:7]
	s_barrier
	ds_read_b128 v[36:39], v207
	ds_read_b128 v[28:31], v207 offset:1024
	ds_read_b128 v[24:27], v207 offset:2048
	ds_read_b128 v[20:23], v207 offset:3072
	ds_read_b128 v[56:59], v208
	ds_read_b128 v[52:55], v208 offset:1024
	ds_read_b128 v[40:43], v208 offset:2048
	ds_read_b128 v[32:35], v208 offset:3072
	ds_read_b128 v[92:95], v206 offset:32768
	ds_read_b128 v[132:135], v206 offset:33792
	ds_read_b128 v[140:143], v206 offset:34816
	ds_read_b128 v[148:151], v206 offset:35840
	ds_read_b128 v[192:195], v206 offset:36864
	ds_read_b128 v[210:213], v206 offset:37888
	ds_read_b128 v[214:217], v206 offset:38912
	ds_read_b128 v[218:221], v206 offset:39936
	s_add_u32 s26, s38, 0x40000
	s_addc_u32 s27, s39, 0
	s_add_i32 m0, s46, 0x4000
	s_nop 0
	global_load_lds_dwordx4 v199, s[26:27]
	s_nop 0
	s_add_i32 m0, s46, 0x6000
	s_nop 0
	global_load_lds_dwordx4 v201, s[26:27]
	s_waitcnt vmcnt(8) lgkmcnt(0)
	s_barrier
	v_mfma_i32_16x16x64_i8 v[156:159], v[36:39], v[92:95], v[184:187]
	v_mfma_i32_16x16x64_i8 v[184:187], v[28:31], v[132:135], v[156:159]
	v_mfma_i32_16x16x64_i8 v[156:159], v[24:27], v[92:95], v[176:179]
	v_mfma_i32_16x16x64_i8 v[176:179], v[20:23], v[132:135], v[156:159]
	v_mfma_i32_16x16x64_i8 v[156:159], v[36:39], v[140:143], v[168:171]
	v_mfma_i32_16x16x64_i8 v[168:171], v[28:31], v[148:151], v[156:159]
	v_mfma_i32_16x16x64_i8 v[156:159], v[24:27], v[140:143], v[160:163]
	v_mfma_i32_16x16x64_i8 v[152:155], v[36:39], v[192:195], v[152:155]
	v_mfma_i32_16x16x64_i8 v[144:147], v[24:27], v[192:195], v[144:147]
	v_mfma_i32_16x16x64_i8 v[136:139], v[36:39], v[214:217], v[136:139]
	v_mfma_i32_16x16x64_i8 v[128:131], v[24:27], v[214:217], v[128:131]
	v_mfma_i32_16x16x64_i8 v[160:163], v[20:23], v[148:151], v[156:159]
	v_mfma_i32_16x16x64_i8 v[152:155], v[28:31], v[210:213], v[152:155]
	v_mfma_i32_16x16x64_i8 v[144:147], v[20:23], v[210:213], v[144:147]
	v_mfma_i32_16x16x64_i8 v[136:139], v[28:31], v[218:221], v[136:139]
	v_mfma_i32_16x16x64_i8 v[128:131], v[20:23], v[218:221], v[128:131]
	v_mfma_i32_16x16x64_i8 v[64:67], v[40:43], v[92:95], v[64:67]
	v_mfma_i32_16x16x64_i8 v[180:183], v[32:35], v[132:135], v[64:67]
	v_mfma_i32_16x16x64_i8 v[64:67], v[56:59], v[140:143], v[68:71]
	v_mfma_i32_16x16x64_i8 v[172:175], v[52:55], v[148:151], v[64:67]
	v_mfma_i32_16x16x64_i8 v[64:67], v[40:43], v[140:143], v[72:75]
	v_mfma_i32_16x16x64_i8 v[156:159], v[56:59], v[92:95], v[188:191]
	v_mfma_i32_16x16x64_i8 v[164:167], v[32:35], v[148:151], v[64:67]
	v_mfma_i32_16x16x64_i8 v[64:67], v[56:59], v[192:195], v[76:79]
	v_mfma_i32_16x16x64_i8 v[188:191], v[52:55], v[132:135], v[156:159]
	v_mfma_i32_16x16x64_i8 v[156:159], v[52:55], v[210:213], v[64:67]
	v_mfma_i32_16x16x64_i8 v[64:67], v[40:43], v[192:195], v[80:83]
	v_mfma_i32_16x16x64_i8 v[148:151], v[32:35], v[210:213], v[64:67]
	v_mfma_i32_16x16x64_i8 v[64:67], v[56:59], v[214:217], v[84:87]
	v_mfma_i32_16x16x64_i8 v[140:143], v[52:55], v[218:221], v[64:67]
	v_mfma_i32_16x16x64_i8 v[64:67], v[40:43], v[214:217], v[88:91]
	v_mfma_i32_16x16x64_i8 v[132:135], v[32:35], v[218:221], v[64:67]
	s_barrier
	ds_read_b128 v[92:95], v206 offset:49152
	ds_read_b128 v[88:91], v206 offset:50176
	ds_read_b128 v[84:87], v206 offset:51200
	ds_read_b128 v[80:83], v206 offset:52224
	ds_read_b128 v[76:79], v206 offset:53248
	ds_read_b128 v[72:75], v206 offset:54272
	ds_read_b128 v[68:71], v206 offset:55296
	ds_read_b128 v[64:67], v206 offset:56320
	s_add_i32 m0, s46, 0x18000
	s_nop 0
	global_load_lds_dwordx4 v200, s[36:37]
	s_nop 0
	s_add_i32 m0, s46, 0x1a000
	s_nop 0
	global_load_lds_dwordx4 v202, s[36:37]
	s_add_u32 s26, s34, 0x40080
	s_addc_u32 s27, s35, 0
	s_add_i32 m0, s46, 0x1c000
	s_nop 0
	global_load_lds_dwordx4 v200, s[26:27]
	s_nop 0
	s_add_i32 m0, s46, 0x1e000
	s_nop 0
	global_load_lds_dwordx4 v202, s[26:27]
	s_nop 0
	s_add_i32 m0, s46, 0x8000
	s_nop 0
	global_load_lds_dwordx4 v199, s[30:31]
	s_nop 0
	s_add_i32 m0, s46, 0xa000
	s_nop 0
	global_load_lds_dwordx4 v201, s[30:31]
	s_add_i32 s17, s17, 2
	s_add_u32 s61, s61, 0x100
	s_addc_u32 s62, s62, 0
	s_cmp_gt_u32 s17, 13
	s_waitcnt vmcnt(8) lgkmcnt(0)
	s_barrier
	v_mfma_i32_16x16x64_i8 v[120:123], v[36:39], v[92:95], v[120:123]
	v_mfma_i32_16x16x64_i8 v[112:115], v[24:27], v[92:95], v[112:115]
	v_mfma_i32_16x16x64_i8 v[96:99], v[24:27], v[84:87], v[96:99]
	v_mfma_i32_16x16x64_i8 v[104:107], v[36:39], v[84:87], v[104:107]
	v_mfma_i32_16x16x64_i8 v[48:51], v[36:39], v[76:79], v[48:51]
	v_mfma_i32_16x16x64_i8 v[16:19], v[24:27], v[76:79], v[16:19]
	v_mfma_i32_16x16x64_i8 v[0:3], v[24:27], v[68:71], v[0:3]
	v_mfma_i32_16x16x64_i8 v[8:11], v[36:39], v[68:71], v[8:11]
	v_mfma_i32_16x16x64_i8 v[120:123], v[28:31], v[88:91], v[120:123]
	v_mfma_i32_16x16x64_i8 v[112:115], v[20:23], v[88:91], v[112:115]
	v_mfma_i32_16x16x64_i8 v[96:99], v[20:23], v[80:83], v[96:99]
	v_mfma_i32_16x16x64_i8 v[104:107], v[28:31], v[80:83], v[104:107]
	v_mfma_i32_16x16x64_i8 v[48:51], v[28:31], v[72:75], v[48:51]
	v_mfma_i32_16x16x64_i8 v[16:19], v[20:23], v[72:75], v[16:19]
	v_mfma_i32_16x16x64_i8 v[0:3], v[20:23], v[64:67], v[0:3]
	v_mfma_i32_16x16x64_i8 v[8:11], v[28:31], v[64:67], v[8:11]
	v_mfma_i32_16x16x64_i8 v[124:127], v[56:59], v[92:95], v[124:127]
	v_mfma_i32_16x16x64_i8 v[116:119], v[40:43], v[92:95], v[116:119]
	v_mfma_i32_16x16x64_i8 v[100:103], v[40:43], v[84:87], v[100:103]
	v_mfma_i32_16x16x64_i8 v[108:111], v[56:59], v[84:87], v[108:111]
	v_mfma_i32_16x16x64_i8 v[60:63], v[56:59], v[76:79], v[60:63]
	v_mfma_i32_16x16x64_i8 v[44:47], v[40:43], v[76:79], v[44:47]
	v_mfma_i32_16x16x64_i8 v[4:7], v[40:43], v[68:71], v[4:7]
	v_mfma_i32_16x16x64_i8 v[12:15], v[56:59], v[68:71], v[12:15]
	v_mfma_i32_16x16x64_i8 v[124:127], v[52:55], v[88:91], v[124:127]
	v_mfma_i32_16x16x64_i8 v[116:119], v[32:35], v[88:91], v[116:119]
	v_mfma_i32_16x16x64_i8 v[100:103], v[32:35], v[80:83], v[100:103]
	v_mfma_i32_16x16x64_i8 v[108:111], v[52:55], v[80:83], v[108:111]
	v_mfma_i32_16x16x64_i8 v[60:63], v[52:55], v[72:75], v[60:63]
	v_mfma_i32_16x16x64_i8 v[44:47], v[32:35], v[72:75], v[44:47]
	v_mfma_i32_16x16x64_i8 v[4:7], v[32:35], v[64:67], v[4:7]
	v_mfma_i32_16x16x64_i8 v[12:15], v[52:55], v[64:67], v[12:15]
	s_barrier
	s_cbranch_scc1 .LBB0_757
	s_mov_b64 s[26:27], s[24:25]
	s_branch .LBB0_753

.LBB0_933:
	ds_read_b128 v[0:3], v227
	ds_read_b128 v[4:7], v227 offset:1024
	ds_read_b128 v[8:11], v227 offset:2048
	ds_read_b128 v[12:15], v227 offset:3072
	ds_read_b128 v[16:19], v226
	ds_read_b128 v[20:23], v226 offset:1024
	ds_read_b128 v[24:27], v226 offset:2048
	ds_read_b128 v[28:31], v226 offset:3072
	ds_read_b128 v[32:35], v228
	ds_read_b128 v[36:39], v228 offset:1024
	ds_read_b128 v[40:43], v228 offset:2048
	ds_read_b128 v[44:47], v228 offset:3072
	ds_read_b128 v[48:51], v228 offset:4096
	ds_read_b128 v[52:55], v228 offset:5120
	ds_read_b128 v[56:59], v228 offset:6144
	ds_read_b128 v[60:63], v228 offset:7168
	s_add_u32 s42, s46, 0x100
	s_addc_u32 s43, s47, 0
	s_and_b64 s[48:49], s[48:49], exec
	s_cselect_b32 s54, s76, s42
	s_cselect_b32 s55, s9, s43
	s_cselect_b32 s51, s35, s80
	s_cselect_b32 s50, s77, s79
	s_add_u32 s48, s54, 0x80
	s_addc_u32 s49, s55, 0
	s_add_u32 s52, s50, 0x80
	s_addc_u32 s53, s51, 0
	s_add_u32 s46, s46, 0x40080
	s_addc_u32 s47, s47, 0
	s_add_i32 m0, s31, 0xc000
	s_nop 0
	global_load_lds_dwordx4 v219, s[46:47]
	s_nop 0
	s_add_i32 m0, s31, 0xe000
	s_nop 0
	global_load_lds_dwordx4 v221, s[46:47]
	s_waitcnt vmcnt(8) lgkmcnt(0)
	s_barrier
	v_mfma_i32_16x16x64_i8 v[180:183], v[8:11], v[40:43], v[180:183]
	v_mfma_i32_16x16x64_i8 v[164:167], v[0:3], v[48:51], v[164:167]
	v_mfma_i32_16x16x64_i8 v[148:151], v[0:3], v[56:59], v[148:151]
	v_mfma_i32_16x16x64_i8 v[160:163], v[8:11], v[48:51], v[160:163]
	v_mfma_i32_16x16x64_i8 v[144:147], v[8:11], v[56:59], v[144:147]
	v_mfma_i32_16x16x64_i8 v[88:91], v[0:3], v[32:35], v[200:203]
	v_mfma_i32_16x16x64_i8 v[168:171], v[0:3], v[40:43], v[184:187]
	v_mfma_i32_16x16x64_i8 v[124:127], v[8:11], v[32:35], v[196:199]
	v_mfma_i32_16x16x64_i8 v[180:183], v[12:15], v[44:47], v[180:183]
	v_mfma_i32_16x16x64_i8 v[164:167], v[4:7], v[52:55], v[164:167]
	v_mfma_i32_16x16x64_i8 v[148:151], v[4:7], v[60:63], v[148:151]
	v_mfma_i32_16x16x64_i8 v[160:163], v[12:15], v[52:55], v[160:163]
	v_mfma_i32_16x16x64_i8 v[144:147], v[12:15], v[60:63], v[144:147]
	v_mfma_i32_16x16x64_i8 v[88:91], v[4:7], v[36:39], v[88:91]
	v_mfma_i32_16x16x64_i8 v[168:171], v[4:7], v[44:47], v[168:171]
	v_mfma_i32_16x16x64_i8 v[124:127], v[12:15], v[36:39], v[124:127]
	v_mfma_i32_16x16x64_i8 v[184:187], v[16:19], v[32:35], v[192:195]
	v_mfma_i32_16x16x64_i8 v[32:35], v[24:27], v[32:35], v[188:191]
	v_mfma_i32_16x16x64_i8 v[192:195], v[20:23], v[36:39], v[184:187]
	v_mfma_i32_16x16x64_i8 v[32:35], v[28:31], v[36:39], v[32:35]
	v_mfma_i32_16x16x64_i8 v[36:39], v[16:19], v[40:43], v[176:179]
	v_mfma_i32_16x16x64_i8 v[40:43], v[24:27], v[40:43], v[172:175]
	v_mfma_i32_16x16x64_i8 v[36:39], v[20:23], v[44:47], v[36:39]
	v_mfma_i32_16x16x64_i8 v[40:43], v[28:31], v[44:47], v[40:43]
	v_mfma_i32_16x16x64_i8 v[44:47], v[16:19], v[48:51], v[156:159]
	v_mfma_i32_16x16x64_i8 v[48:51], v[24:27], v[48:51], v[152:155]
	v_mfma_i32_16x16x64_i8 v[44:47], v[20:23], v[52:55], v[44:47]
	v_mfma_i32_16x16x64_i8 v[48:51], v[28:31], v[52:55], v[48:51]
	v_mfma_i32_16x16x64_i8 v[52:55], v[16:19], v[56:59], v[140:143]
	v_mfma_i32_16x16x64_i8 v[56:59], v[24:27], v[56:59], v[136:139]
	v_mfma_i32_16x16x64_i8 v[52:55], v[20:23], v[60:63], v[52:55]
	v_mfma_i32_16x16x64_i8 v[56:59], v[28:31], v[60:63], v[56:59]
	s_barrier
	ds_read_b128 v[60:63], v228 offset:16384
	ds_read_b128 v[136:139], v228 offset:17408
	ds_read_b128 v[140:143], v228 offset:18432
	ds_read_b128 v[152:155], v228 offset:19456
	ds_read_b128 v[156:159], v228 offset:20480
	ds_read_b128 v[172:175], v228 offset:21504
	ds_read_b128 v[176:179], v228 offset:22528
	ds_read_b128 v[184:187], v228 offset:23552
	s_add_i32 m0, s31, 0x10000
	s_nop 0
	global_load_lds_dwordx4 v220, s[50:51]
	s_nop 0
	s_add_i32 m0, s31, 0x12000
	s_nop 0
	global_load_lds_dwordx4 v222, s[50:51]
	s_add_u32 s46, s50, 0x40000
	s_addc_u32 s47, s51, 0
	s_add_i32 m0, s31, 0x14000
	s_nop 0
	global_load_lds_dwordx4 v220, s[46:47]
	s_nop 0
	s_add_i32 m0, s31, 0x16000
	s_nop 0
	global_load_lds_dwordx4 v222, s[46:47]
	s_nop 0
	s_add_i32 m0, s31, 0
	s_nop 0
	global_load_lds_dwordx4 v219, s[54:55]
	s_nop 0
	s_add_i32 m0, s31, 0x2000
	s_nop 0
	global_load_lds_dwordx4 v221, s[54:55]
	s_waitcnt vmcnt(8) lgkmcnt(0)
	s_barrier
	v_mfma_i32_16x16x64_i8 v[132:135], v[0:3], v[60:63], v[132:135]
	v_mfma_i32_16x16x64_i8 v[112:115], v[0:3], v[140:143], v[112:115]
	v_mfma_i32_16x16x64_i8 v[96:99], v[0:3], v[156:159], v[96:99]
	v_mfma_i32_16x16x64_i8 v[0:3], v[0:3], v[176:179], v[76:79]
	v_mfma_i32_16x16x64_i8 v[128:131], v[8:11], v[60:63], v[128:131]
	v_mfma_i32_16x16x64_i8 v[108:111], v[8:11], v[140:143], v[108:111]
	v_mfma_i32_16x16x64_i8 v[92:95], v[8:11], v[156:159], v[92:95]
	v_mfma_i32_16x16x64_i8 v[76:79], v[4:7], v[184:187], v[0:3]
	v_mfma_i32_16x16x64_i8 v[0:3], v[8:11], v[176:179], v[72:75]
	v_mfma_i32_16x16x64_i8 v[132:135], v[4:7], v[136:139], v[132:135]
	v_mfma_i32_16x16x64_i8 v[128:131], v[12:15], v[136:139], v[128:131]
	v_mfma_i32_16x16x64_i8 v[112:115], v[4:7], v[152:155], v[112:115]
	v_mfma_i32_16x16x64_i8 v[108:111], v[12:15], v[152:155], v[108:111]
	v_mfma_i32_16x16x64_i8 v[96:99], v[4:7], v[172:175], v[96:99]
	v_mfma_i32_16x16x64_i8 v[92:95], v[12:15], v[172:175], v[92:95]
	v_mfma_i32_16x16x64_i8 v[72:75], v[12:15], v[184:187], v[0:3]
	v_mfma_i32_16x16x64_i8 v[0:3], v[16:19], v[60:63], v[120:123]
	v_mfma_i32_16x16x64_i8 v[120:123], v[20:23], v[136:139], v[0:3]
	v_mfma_i32_16x16x64_i8 v[0:3], v[24:27], v[60:63], v[116:119]
	v_mfma_i32_16x16x64_i8 v[116:119], v[28:31], v[136:139], v[0:3]
	v_mfma_i32_16x16x64_i8 v[0:3], v[16:19], v[140:143], v[104:107]
	v_mfma_i32_16x16x64_i8 v[104:107], v[20:23], v[152:155], v[0:3]
	v_mfma_i32_16x16x64_i8 v[0:3], v[24:27], v[140:143], v[100:103]
	v_mfma_i32_16x16x64_i8 v[100:103], v[28:31], v[152:155], v[0:3]
	v_mfma_i32_16x16x64_i8 v[0:3], v[16:19], v[156:159], v[84:87]
	v_mfma_i32_16x16x64_i8 v[84:87], v[20:23], v[172:175], v[0:3]
	v_mfma_i32_16x16x64_i8 v[0:3], v[24:27], v[156:159], v[80:83]
	v_mfma_i32_16x16x64_i8 v[80:83], v[28:31], v[172:175], v[0:3]
	v_mfma_i32_16x16x64_i8 v[0:3], v[16:19], v[176:179], v[68:71]
	v_mfma_i32_16x16x64_i8 v[68:71], v[20:23], v[184:187], v[0:3]
	v_mfma_i32_16x16x64_i8 v[0:3], v[24:27], v[176:179], v[64:67]
	v_mfma_i32_16x16x64_i8 v[64:67], v[28:31], v[184:187], v[0:3]
	s_barrier
	ds_read_b128 v[16:19], v229
	ds_read_b128 v[8:11], v229 offset:1024
	ds_read_b128 v[4:7], v229 offset:2048
	s_nop 1
	ds_read_b128 v[0:3], v229 offset:3072
	ds_read_b128 v[28:31], v230
	ds_read_b128 v[24:27], v230 offset:1024
	ds_read_b128 v[20:23], v230 offset:2048
	ds_read_b128 v[12:15], v230 offset:3072
	ds_read_b128 v[60:63], v228 offset:32768
	ds_read_b128 v[136:139], v228 offset:33792
	ds_read_b128 v[140:143], v228 offset:34816
	ds_read_b128 v[152:155], v228 offset:35840
	ds_read_b128 v[204:207], v228 offset:36864
	ds_read_b128 v[208:211], v228 offset:37888
	ds_read_b128 v[214:217], v228 offset:38912
	ds_read_b128 v[232:235], v228 offset:39936
	s_add_u32 s46, s54, 0x40000
	s_addc_u32 s47, s55, 0
	s_add_i32 m0, s31, 0x4000
	s_nop 0
	global_load_lds_dwordx4 v219, s[46:47]
	s_nop 0
	s_add_i32 m0, s31, 0x6000
	s_nop 0
	global_load_lds_dwordx4 v221, s[46:47]
	s_waitcnt vmcnt(8) lgkmcnt(0)
	s_barrier
	v_mfma_i32_16x16x64_i8 v[88:91], v[16:19], v[60:63], v[88:91]
	v_mfma_i32_16x16x64_i8 v[200:203], v[8:11], v[136:139], v[88:91]
	v_mfma_i32_16x16x64_i8 v[88:91], v[4:7], v[60:63], v[124:127]
	v_mfma_i32_16x16x64_i8 v[196:199], v[0:3], v[136:139], v[88:91]
	v_mfma_i32_16x16x64_i8 v[88:91], v[16:19], v[140:143], v[168:171]
	v_mfma_i32_16x16x64_i8 v[184:187], v[8:11], v[152:155], v[88:91]
	v_mfma_i32_16x16x64_i8 v[88:91], v[4:7], v[140:143], v[180:183]
	v_mfma_i32_16x16x64_i8 v[180:183], v[0:3], v[152:155], v[88:91]
	v_mfma_i32_16x16x64_i8 v[88:91], v[16:19], v[204:207], v[164:167]
	v_mfma_i32_16x16x64_i8 v[164:167], v[8:11], v[208:211], v[88:91]
	v_mfma_i32_16x16x64_i8 v[88:91], v[4:7], v[204:207], v[160:163]
	v_mfma_i32_16x16x64_i8 v[160:163], v[0:3], v[208:211], v[88:91]
	v_mfma_i32_16x16x64_i8 v[88:91], v[16:19], v[214:217], v[148:151]
	v_mfma_i32_16x16x64_i8 v[148:151], v[8:11], v[232:235], v[88:91]
	v_mfma_i32_16x16x64_i8 v[88:91], v[4:7], v[214:217], v[144:147]
	v_mfma_i32_16x16x64_i8 v[144:147], v[0:3], v[232:235], v[88:91]
	v_mfma_i32_16x16x64_i8 v[32:35], v[20:23], v[60:63], v[32:35]
	v_mfma_i32_16x16x64_i8 v[188:191], v[12:15], v[136:139], v[32:35]
	v_mfma_i32_16x16x64_i8 v[32:35], v[28:31], v[140:143], v[36:39]
	v_mfma_i32_16x16x64_i8 v[176:179], v[24:27], v[152:155], v[32:35]
	v_mfma_i32_16x16x64_i8 v[32:35], v[20:23], v[140:143], v[40:43]
	v_mfma_i32_16x16x64_i8 v[172:175], v[12:15], v[152:155], v[32:35]
	v_mfma_i32_16x16x64_i8 v[32:35], v[28:31], v[204:207], v[44:47]
	v_mfma_i32_16x16x64_i8 v[156:159], v[24:27], v[208:211], v[32:35]
	v_mfma_i32_16x16x64_i8 v[32:35], v[20:23], v[204:207], v[48:51]
	v_mfma_i32_16x16x64_i8 v[152:155], v[12:15], v[208:211], v[32:35]
	v_mfma_i32_16x16x64_i8 v[32:35], v[28:31], v[214:217], v[52:55]
	v_mfma_i32_16x16x64_i8 v[88:91], v[28:31], v[60:63], v[192:195]
	v_mfma_i32_16x16x64_i8 v[140:143], v[24:27], v[232:235], v[32:35]
	v_mfma_i32_16x16x64_i8 v[32:35], v[20:23], v[214:217], v[56:59]
	v_mfma_i32_16x16x64_i8 v[192:195], v[24:27], v[136:139], v[88:91]
	v_mfma_i32_16x16x64_i8 v[136:139], v[12:15], v[232:235], v[32:35]
	s_barrier
	ds_read_b128 v[60:63], v228 offset:49152
	ds_read_b128 v[56:59], v228 offset:50176
	ds_read_b128 v[52:55], v228 offset:51200
	ds_read_b128 v[48:51], v228 offset:52224
	ds_read_b128 v[44:47], v228 offset:53248
	ds_read_b128 v[40:43], v228 offset:54272
	ds_read_b128 v[36:39], v228 offset:55296
	ds_read_b128 v[32:35], v228 offset:56320
	s_add_i32 m0, s31, 0x18000
	s_nop 0
	global_load_lds_dwordx4 v220, s[52:53]
	s_nop 0
	s_add_i32 m0, s31, 0x1a000
	s_nop 0
	global_load_lds_dwordx4 v222, s[52:53]
	s_add_u32 s46, s50, 0x40080
	s_addc_u32 s47, s51, 0
	s_add_i32 m0, s31, 0x1c000
	s_nop 0
	global_load_lds_dwordx4 v220, s[46:47]
	s_nop 0
	s_add_i32 m0, s31, 0x1e000
	s_nop 0
	global_load_lds_dwordx4 v222, s[46:47]
	s_nop 0
	s_add_i32 m0, s31, 0x8000
	s_nop 0
	global_load_lds_dwordx4 v219, s[48:49]
	s_nop 0
	s_add_i32 m0, s31, 0xa000
	s_nop 0
	global_load_lds_dwordx4 v221, s[48:49]
	s_add_i32 s37, s37, 2
	s_add_u32 s79, s79, 0x100
	s_addc_u32 s80, s80, 0
	s_cmp_gt_u32 s37, 13
	s_waitcnt vmcnt(8) lgkmcnt(0)
	s_barrier
	v_mfma_i32_16x16x64_i8 v[88:91], v[16:19], v[60:63], v[132:135]
	v_mfma_i32_16x16x64_i8 v[132:135], v[8:11], v[56:59], v[88:91]
	v_mfma_i32_16x16x64_i8 v[88:91], v[4:7], v[60:63], v[128:131]
	v_mfma_i32_16x16x64_i8 v[128:131], v[0:3], v[56:59], v[88:91]
	v_mfma_i32_16x16x64_i8 v[88:91], v[16:19], v[52:55], v[112:115]
	v_mfma_i32_16x16x64_i8 v[112:115], v[8:11], v[48:51], v[88:91]
	v_mfma_i32_16x16x64_i8 v[88:91], v[4:7], v[52:55], v[108:111]
	v_mfma_i32_16x16x64_i8 v[108:111], v[0:3], v[48:51], v[88:91]
	v_mfma_i32_16x16x64_i8 v[88:91], v[16:19], v[44:47], v[96:99]
	v_mfma_i32_16x16x64_i8 v[96:99], v[8:11], v[40:43], v[88:91]
	v_mfma_i32_16x16x64_i8 v[88:91], v[4:7], v[44:47], v[92:95]
	v_mfma_i32_16x16x64_i8 v[76:79], v[16:19], v[36:39], v[76:79]
	v_mfma_i32_16x16x64_i8 v[72:75], v[4:7], v[36:39], v[72:75]
	v_mfma_i32_16x16x64_i8 v[92:95], v[0:3], v[40:43], v[88:91]
	v_mfma_i32_16x16x64_i8 v[76:79], v[8:11], v[32:35], v[76:79]
	v_mfma_i32_16x16x64_i8 v[72:75], v[0:3], v[32:35], v[72:75]
	v_mfma_i32_16x16x64_i8 v[88:91], v[28:31], v[60:63], v[120:123]
	v_mfma_i32_16x16x64_i8 v[120:123], v[24:27], v[56:59], v[88:91]
	v_mfma_i32_16x16x64_i8 v[88:91], v[20:23], v[60:63], v[116:119]
	v_mfma_i32_16x16x64_i8 v[116:119], v[12:15], v[56:59], v[88:91]
	v_mfma_i32_16x16x64_i8 v[88:91], v[28:31], v[52:55], v[104:107]
	v_mfma_i32_16x16x64_i8 v[104:107], v[24:27], v[48:51], v[88:91]
	v_mfma_i32_16x16x64_i8 v[88:91], v[20:23], v[52:55], v[100:103]
	v_mfma_i32_16x16x64_i8 v[84:87], v[28:31], v[44:47], v[84:87]
	v_mfma_i32_16x16x64_i8 v[80:83], v[20:23], v[44:47], v[80:83]
	v_mfma_i32_16x16x64_i8 v[68:71], v[28:31], v[36:39], v[68:71]
	v_mfma_i32_16x16x64_i8 v[64:67], v[20:23], v[36:39], v[64:67]
	v_mfma_i32_16x16x64_i8 v[100:103], v[12:15], v[48:51], v[88:91]
	v_mfma_i32_16x16x64_i8 v[84:87], v[24:27], v[40:43], v[84:87]
	v_mfma_i32_16x16x64_i8 v[80:83], v[12:15], v[40:43], v[80:83]
	v_mfma_i32_16x16x64_i8 v[68:71], v[24:27], v[32:35], v[68:71]
	v_mfma_i32_16x16x64_i8 v[64:67], v[12:15], v[32:35], v[64:67]
	s_barrier
	s_cbranch_scc1 .LBB0_935
	s_mov_b64 s[46:47], s[42:43]
	s_branch .LBB0_931

.LBB0_1411:
	ds_read_b128 v[146:149], v138
	ds_read_b128 v[150:153], v138 offset:1024
	ds_read_b128 v[154:157], v138 offset:2048
	ds_read_b128 v[158:161], v138 offset:3072
	ds_read_b128 v[162:165], v139
	ds_read_b128 v[166:169], v139 offset:1024
	ds_read_b128 v[170:173], v139 offset:2048
	ds_read_b128 v[174:177], v139 offset:3072
	ds_read_b128 v[178:181], v140
	ds_read_b128 v[182:185], v140 offset:1024
	ds_read_b128 v[186:189], v140 offset:2048
	ds_read_b128 v[190:193], v140 offset:3072
	ds_read_b128 v[194:197], v140 offset:4096
	ds_read_b128 v[198:201], v140 offset:5120
	ds_read_b128 v[202:205], v140 offset:6144
	ds_read_b128 v[206:209], v140 offset:7168
	s_add_u32 s26, s6, 0x100
	s_addc_u32 s27, s7, 0
	s_cmp_eq_u32 s55, 12
	s_cselect_b32 s36, s15, s26
	s_cselect_b32 s37, s2, s27
	s_cselect_b32 s30, s18, s17
	s_cselect_b32 s31, s19, s54
	s_add_u32 s28, s36, 0x80
	s_addc_u32 s29, s37, 0
	s_add_u32 s34, s30, 0x80
	s_addc_u32 s35, s31, 0
	s_add_u32 s6, s6, 0x40080
	s_addc_u32 s7, s7, 0
	s_add_i32 m0, s47, 0xc000
	s_nop 0
	global_load_lds_dwordx4 v134, s[6:7]
	s_nop 0
	s_add_i32 m0, s47, 0xe000
	s_nop 0
	global_load_lds_dwordx4 v136, s[6:7]
	s_waitcnt vmcnt(8) lgkmcnt(0)
	s_barrier
	v_mfma_f32_16x16x128_f8f6f4 v[112:115], v[146:153], v[178:185], v[112:115]
	v_mfma_f32_16x16x128_f8f6f4 v[116:119], v[154:161], v[178:185], v[116:119]
	v_mfma_f32_16x16x128_f8f6f4 v[96:99], v[154:161], v[186:193], v[96:99]
	v_mfma_f32_16x16x128_f8f6f4 v[100:103], v[146:153], v[186:193], v[100:103]
	v_mfma_f32_16x16x128_f8f6f4 v[210:213], v[146:153], v[194:201], v[84:87]
	v_mfma_f32_16x16x128_f8f6f4 v[214:217], v[154:161], v[194:201], v[80:83]
	v_mfma_f32_16x16x128_f8f6f4 v[222:225], v[154:161], v[202:209], v[56:59]
	v_mfma_f32_16x16x128_f8f6f4 v[218:221], v[146:153], v[202:209], v[60:63]
	v_mfma_f32_16x16x128_f8f6f4 v[120:123], v[162:169], v[178:185], v[120:123]
	v_mfma_f32_16x16x128_f8f6f4 v[124:127], v[170:177], v[178:185], v[124:127]
	v_mfma_f32_16x16x128_f8f6f4 v[108:111], v[162:169], v[186:193], v[108:111]
	v_mfma_f32_16x16x128_f8f6f4 v[104:107], v[170:177], v[186:193], v[104:107]
	v_mfma_f32_16x16x128_f8f6f4 v[178:181], v[162:169], v[194:201], v[92:95]
	v_mfma_f32_16x16x128_f8f6f4 v[182:185], v[170:177], v[194:201], v[88:91]
	v_mfma_f32_16x16x128_f8f6f4 v[186:189], v[162:169], v[202:209], v[76:79]
	v_mfma_f32_16x16x128_f8f6f4 v[190:193], v[170:177], v[202:209], v[72:75]
	s_barrier
	ds_read_b128 v[56:59], v140 offset:16384
	ds_read_b128 v[60:63], v140 offset:17408
	s_nop 2
	ds_read_b128 v[72:75], v140 offset:18432
	ds_read_b128 v[76:79], v140 offset:19456
	ds_read_b128 v[80:83], v140 offset:20480
	ds_read_b128 v[84:87], v140 offset:21504
	ds_read_b128 v[88:91], v140 offset:22528
	ds_read_b128 v[92:95], v140 offset:23552
	s_add_i32 m0, s47, 0x10000
	s_nop 0
	global_load_lds_dwordx4 v135, s[30:31]
	s_nop 0
	s_add_i32 m0, s47, 0x12000
	s_nop 0
	global_load_lds_dwordx4 v137, s[30:31]
	s_add_u32 s6, s30, 0x40000
	s_addc_u32 s7, s31, 0
	s_add_i32 m0, s47, 0x14000
	s_nop 0
	global_load_lds_dwordx4 v135, s[6:7]
	s_nop 0
	s_add_i32 m0, s47, 0x16000
	s_nop 0
	global_load_lds_dwordx4 v137, s[6:7]
	s_nop 0
	s_add_i32 m0, s47, 0
	s_nop 0
	global_load_lds_dwordx4 v134, s[36:37]
	s_nop 0
	s_add_i32 m0, s47, 0x2000
	s_nop 0
	global_load_lds_dwordx4 v136, s[36:37]
	s_waitcnt vmcnt(8) lgkmcnt(0)
	s_barrier
	v_mfma_f32_16x16x128_f8f6f4 v[52:55], v[146:153], v[56:63], v[52:55]
	v_mfma_f32_16x16x128_f8f6f4 v[48:51], v[154:161], v[56:63], v[48:51]
	v_mfma_f32_16x16x128_f8f6f4 v[198:201], v[154:161], v[72:79], v[32:35]
	v_mfma_f32_16x16x128_f8f6f4 v[194:197], v[146:153], v[72:79], v[36:39]
	v_mfma_f32_16x16x128_f8f6f4 v[202:205], v[146:153], v[80:87], v[20:23]
	v_mfma_f32_16x16x128_f8f6f4 v[206:209], v[154:161], v[80:87], v[16:19]
	v_mfma_f32_16x16x128_f8f6f4 v[230:233], v[154:161], v[88:95], v[0:3]
	v_mfma_f32_16x16x128_f8f6f4 v[226:229], v[146:153], v[88:95], v[4:7]
	v_mfma_f32_16x16x128_f8f6f4 v[68:71], v[162:169], v[56:63], v[68:71]
	v_mfma_f32_16x16x128_f8f6f4 v[64:67], v[170:177], v[56:63], v[64:67]
	v_mfma_f32_16x16x128_f8f6f4 v[238:241], v[170:177], v[72:79], v[40:43]
	v_mfma_f32_16x16x128_f8f6f4 v[234:237], v[162:169], v[72:79], v[44:47]
	v_mfma_f32_16x16x128_f8f6f4 v[242:245], v[162:169], v[80:87], v[28:31]
	v_mfma_f32_16x16x128_f8f6f4 v[246:249], v[170:177], v[80:87], v[24:27]
	v_mfma_f32_16x16x128_f8f6f4 v[130:133], v[170:177], v[88:95], v[8:11]
	v_mfma_f32_16x16x128_f8f6f4 v[250:253], v[162:169], v[88:95], v[12:15]
	s_barrier
	ds_read_b128 v[0:3], v141
	ds_read_b128 v[4:7], v141 offset:1024
	s_nop 2
	ds_read_b128 v[8:11], v141 offset:2048
	ds_read_b128 v[12:15], v141 offset:3072
	ds_read_b128 v[146:149], v142
	ds_read_b128 v[150:153], v142 offset:1024
	ds_read_b128 v[154:157], v142 offset:2048
	ds_read_b128 v[158:161], v142 offset:3072
	ds_read_b128 v[16:19], v140 offset:32768
	ds_read_b128 v[20:23], v140 offset:33792
	ds_read_b128 v[24:27], v140 offset:34816
	ds_read_b128 v[28:31], v140 offset:35840
	ds_read_b128 v[32:35], v140 offset:36864
	ds_read_b128 v[36:39], v140 offset:37888
	ds_read_b128 v[40:43], v140 offset:38912
	ds_read_b128 v[44:47], v140 offset:39936
	s_add_u32 s6, s36, 0x40000
	s_addc_u32 s7, s37, 0
	s_add_i32 m0, s47, 0x4000
	s_nop 0
	global_load_lds_dwordx4 v134, s[6:7]
	s_nop 0
	s_add_i32 m0, s47, 0x6000
	s_nop 0
	global_load_lds_dwordx4 v136, s[6:7]
	s_waitcnt vmcnt(8) lgkmcnt(0)
	s_barrier
	v_mfma_f32_16x16x128_f8f6f4 v[112:115], v[0:7], v[16:23], v[112:115]
	v_mfma_f32_16x16x128_f8f6f4 v[116:119], v[8:15], v[16:23], v[116:119]
	v_mfma_f32_16x16x128_f8f6f4 v[96:99], v[8:15], v[24:31], v[96:99]
	v_mfma_f32_16x16x128_f8f6f4 v[100:103], v[0:7], v[24:31], v[100:103]
	v_mfma_f32_16x16x128_f8f6f4 v[84:87], v[0:7], v[32:39], v[210:213]
	v_mfma_f32_16x16x128_f8f6f4 v[80:83], v[8:15], v[32:39], v[214:217]
	v_mfma_f32_16x16x128_f8f6f4 v[56:59], v[8:15], v[40:47], v[222:225]
	v_mfma_f32_16x16x128_f8f6f4 v[60:63], v[0:7], v[40:47], v[218:221]
	v_mfma_f32_16x16x128_f8f6f4 v[120:123], v[146:153], v[16:23], v[120:123]
	v_mfma_f32_16x16x128_f8f6f4 v[124:127], v[154:161], v[16:23], v[124:127]
	v_mfma_f32_16x16x128_f8f6f4 v[104:107], v[154:161], v[24:31], v[104:107]
	v_mfma_f32_16x16x128_f8f6f4 v[108:111], v[146:153], v[24:31], v[108:111]
	v_mfma_f32_16x16x128_f8f6f4 v[92:95], v[146:153], v[32:39], v[178:181]
	v_mfma_f32_16x16x128_f8f6f4 v[88:91], v[154:161], v[32:39], v[182:185]
	v_mfma_f32_16x16x128_f8f6f4 v[72:75], v[154:161], v[40:47], v[190:193]
	v_mfma_f32_16x16x128_f8f6f4 v[76:79], v[146:153], v[40:47], v[186:189]
	s_barrier
	ds_read_b128 v[24:27], v140 offset:49152
	ds_read_b128 v[28:31], v140 offset:50176
	ds_read_b128 v[162:165], v140 offset:51200
	ds_read_b128 v[166:169], v140 offset:52224
	ds_read_b128 v[170:173], v140 offset:53248
	ds_read_b128 v[174:177], v140 offset:54272
	ds_read_b128 v[178:181], v140 offset:55296
	ds_read_b128 v[182:185], v140 offset:56320
	s_add_i32 m0, s47, 0x18000
	s_nop 0
	global_load_lds_dwordx4 v135, s[34:35]
	s_nop 0
	s_add_i32 m0, s47, 0x1a000
	s_nop 0
	global_load_lds_dwordx4 v137, s[34:35]
	s_add_u32 s6, s30, 0x40080
	s_addc_u32 s7, s31, 0
	s_add_i32 m0, s47, 0x1c000
	s_nop 0
	global_load_lds_dwordx4 v135, s[6:7]
	s_nop 0
	s_add_i32 m0, s47, 0x1e000
	s_nop 0
	global_load_lds_dwordx4 v137, s[6:7]
	s_nop 0
	s_add_i32 m0, s47, 0x8000
	s_nop 0
	global_load_lds_dwordx4 v134, s[28:29]
	s_nop 0
	s_add_i32 m0, s47, 0xa000
	s_nop 0
	global_load_lds_dwordx4 v136, s[28:29]
	s_add_i32 s55, s55, 2
	s_add_u32 s17, s17, 0x100
	s_addc_u32 s54, s54, 0
	s_cmp_gt_u32 s55, 13
	s_mov_b64 s[6:7], s[26:27]
	s_waitcnt vmcnt(8) lgkmcnt(0)
	s_barrier
	v_mfma_f32_16x16x128_f8f6f4 v[52:55], v[0:7], v[24:31], v[52:55]
	v_mfma_f32_16x16x128_f8f6f4 v[48:51], v[8:15], v[24:31], v[48:51]
	v_mfma_f32_16x16x128_f8f6f4 v[36:39], v[0:7], v[162:169], v[194:197]
	v_mfma_f32_16x16x128_f8f6f4 v[32:35], v[8:15], v[162:169], v[198:201]
	v_mfma_f32_16x16x128_f8f6f4 v[20:23], v[0:7], v[170:177], v[202:205]
	v_mfma_f32_16x16x128_f8f6f4 v[16:19], v[8:15], v[170:177], v[206:209]
	v_mfma_f32_16x16x128_f8f6f4 v[4:7], v[0:7], v[178:185], v[226:229]
	v_mfma_f32_16x16x128_f8f6f4 v[0:3], v[8:15], v[178:185], v[230:233]
	v_mfma_f32_16x16x128_f8f6f4 v[68:71], v[146:153], v[24:31], v[68:71]
	v_mfma_f32_16x16x128_f8f6f4 v[64:67], v[154:161], v[24:31], v[64:67]
	v_mfma_f32_16x16x128_f8f6f4 v[44:47], v[146:153], v[162:169], v[234:237]
	v_mfma_f32_16x16x128_f8f6f4 v[40:43], v[154:161], v[162:169], v[238:241]
	v_mfma_f32_16x16x128_f8f6f4 v[28:31], v[146:153], v[170:177], v[242:245]
	v_mfma_f32_16x16x128_f8f6f4 v[24:27], v[154:161], v[170:177], v[246:249]
	v_mfma_f32_16x16x128_f8f6f4 v[12:15], v[146:153], v[178:185], v[250:253]
	v_mfma_f32_16x16x128_f8f6f4 v[8:11], v[154:161], v[178:185], v[130:133]
	s_barrier
	s_cbranch_scc0 .LBB0_1411
	s_and_b64 vcc, exec, s[12:13]
	s_cbranch_vccz .LBB0_1414
	s_barrier

.LBB0_1488:
	ds_read_b128 v[132:135], v153
	ds_read_b128 v[136:139], v153 offset:1024
	ds_read_b128 v[140:143], v153 offset:2048
	ds_read_b128 v[144:147], v153 offset:3072
	ds_read_b128 v[158:161], v154
	ds_read_b128 v[162:165], v154 offset:1024
	ds_read_b128 v[166:169], v154 offset:2048
	ds_read_b128 v[170:173], v154 offset:3072
	ds_read_b128 v[174:177], v155
	ds_read_b128 v[178:181], v155 offset:1024
	ds_read_b128 v[182:185], v155 offset:2048
	ds_read_b128 v[186:189], v155 offset:3072
	ds_read_b128 v[190:193], v155 offset:4096
	ds_read_b128 v[194:197], v155 offset:5120
	ds_read_b128 v[198:201], v155 offset:6144
	ds_read_b128 v[202:205], v155 offset:7168
	s_add_u32 s24, s26, 0x100
	s_addc_u32 s25, s27, 0
	s_cmp_eq_u32 s52, 52
	s_cselect_b32 s36, s6, s24
	s_cselect_b32 s37, s7, s25
	s_cselect_b32 s30, s20, s23
	s_cselect_b32 s31, s21, s51
	s_add_u32 s28, s36, 0x80
	s_addc_u32 s29, s37, 0
	s_add_u32 s34, s30, 0x80
	s_addc_u32 s35, s31, 0
	s_add_u32 s26, s26, 0xe0080
	s_addc_u32 s27, s27, 0
	s_add_i32 m0, s44, 0xc000
	s_nop 0
	global_load_lds_dwordx4 v149, s[26:27]
	s_nop 0
	s_add_i32 m0, s44, 0xe000
	s_nop 0
	global_load_lds_dwordx4 v151, s[26:27]
	s_waitcnt vmcnt(8) lgkmcnt(0)
	s_barrier
	v_mfma_f32_16x16x128_f8f6f4 v[112:115], v[132:139], v[174:181], v[112:115]
	v_mfma_f32_16x16x128_f8f6f4 v[116:119], v[140:147], v[174:181], v[116:119]
	v_mfma_f32_16x16x128_f8f6f4 v[96:99], v[140:147], v[182:189], v[96:99]
	v_mfma_f32_16x16x128_f8f6f4 v[100:103], v[132:139], v[182:189], v[100:103]
	v_mfma_f32_16x16x128_f8f6f4 v[206:209], v[132:139], v[190:197], v[84:87]
	v_mfma_f32_16x16x128_f8f6f4 v[210:213], v[140:147], v[190:197], v[80:83]
	v_mfma_f32_16x16x128_f8f6f4 v[218:221], v[140:147], v[198:205], v[52:55]
	v_mfma_f32_16x16x128_f8f6f4 v[214:217], v[132:139], v[198:205], v[60:63]
	v_mfma_f32_16x16x128_f8f6f4 v[120:123], v[158:165], v[174:181], v[120:123]
	v_mfma_f32_16x16x128_f8f6f4 v[124:127], v[166:173], v[174:181], v[124:127]
	v_mfma_f32_16x16x128_f8f6f4 v[108:111], v[158:165], v[182:189], v[108:111]
	v_mfma_f32_16x16x128_f8f6f4 v[104:107], v[166:173], v[182:189], v[104:107]
	v_mfma_f32_16x16x128_f8f6f4 v[174:177], v[158:165], v[190:197], v[92:95]
	v_mfma_f32_16x16x128_f8f6f4 v[178:181], v[166:173], v[190:197], v[88:91]
	v_mfma_f32_16x16x128_f8f6f4 v[182:185], v[158:165], v[198:205], v[56:59]
	v_mfma_f32_16x16x128_f8f6f4 v[186:189], v[166:173], v[198:205], v[48:51]
	s_barrier
	s_nop 4
	ds_read_b128 v[48:51], v155 offset:16384
	ds_read_b128 v[52:55], v155 offset:17408
	ds_read_b128 v[56:59], v155 offset:18432
	ds_read_b128 v[60:63], v155 offset:19456
	ds_read_b128 v[80:83], v155 offset:20480
	ds_read_b128 v[84:87], v155 offset:21504
	ds_read_b128 v[88:91], v155 offset:22528
	ds_read_b128 v[92:95], v155 offset:23552
	s_add_i32 m0, s44, 0x10000
	s_nop 0
	global_load_lds_dwordx4 v150, s[30:31]
	s_nop 0
	s_add_i32 m0, s44, 0x12000
	s_nop 0
	global_load_lds_dwordx4 v152, s[30:31]
	s_add_u32 s26, s30, 0xe0000
	s_addc_u32 s27, s31, 0
	s_add_i32 m0, s44, 0x14000
	s_nop 0
	global_load_lds_dwordx4 v150, s[26:27]
	s_nop 0
	s_add_i32 m0, s44, 0x16000
	s_nop 0
	global_load_lds_dwordx4 v152, s[26:27]
	s_nop 0
	s_add_i32 m0, s44, 0
	s_nop 0
	global_load_lds_dwordx4 v149, s[36:37]
	s_nop 0
	s_add_i32 m0, s44, 0x2000
	s_nop 0
	global_load_lds_dwordx4 v151, s[36:37]
	s_waitcnt vmcnt(8) lgkmcnt(0)
	s_barrier
	v_mfma_f32_16x16x128_f8f6f4 v[68:71], v[132:139], v[48:55], v[68:71]
	v_mfma_f32_16x16x128_f8f6f4 v[64:67], v[140:147], v[48:55], v[64:67]
	v_mfma_f32_16x16x128_f8f6f4 v[194:197], v[140:147], v[56:63], v[36:39]
	v_mfma_f32_16x16x128_f8f6f4 v[190:193], v[132:139], v[56:63], v[44:47]
	v_mfma_f32_16x16x128_f8f6f4 v[198:201], v[132:139], v[80:87], v[28:31]
	v_mfma_f32_16x16x128_f8f6f4 v[202:205], v[140:147], v[80:87], v[24:27]
	v_mfma_f32_16x16x128_f8f6f4 v[226:229], v[140:147], v[88:95], v[8:11]
	v_mfma_f32_16x16x128_f8f6f4 v[222:225], v[132:139], v[88:95], v[12:15]
	v_mfma_f32_16x16x128_f8f6f4 v[76:79], v[158:165], v[48:55], v[76:79]
	v_mfma_f32_16x16x128_f8f6f4 v[72:75], v[166:173], v[48:55], v[72:75]
	v_mfma_f32_16x16x128_f8f6f4 v[234:237], v[166:173], v[56:63], v[32:35]
	v_mfma_f32_16x16x128_f8f6f4 v[230:233], v[158:165], v[56:63], v[40:43]
	v_mfma_f32_16x16x128_f8f6f4 v[238:241], v[158:165], v[80:87], v[20:23]
	v_mfma_f32_16x16x128_f8f6f4 v[242:245], v[166:173], v[80:87], v[16:19]
	v_mfma_f32_16x16x128_f8f6f4 v[250:253], v[166:173], v[88:95], v[0:3]
	v_mfma_f32_16x16x128_f8f6f4 v[246:249], v[158:165], v[88:95], v[4:7]
	s_barrier
	s_nop 4
	ds_read_b128 v[0:3], v156
	ds_read_b128 v[4:7], v156 offset:1024
	ds_read_b128 v[16:19], v156 offset:2048
	ds_read_b128 v[20:23], v156 offset:3072
	ds_read_b128 v[132:135], v157
	ds_read_b128 v[136:139], v157 offset:1024
	ds_read_b128 v[140:143], v157 offset:2048
	ds_read_b128 v[144:147], v157 offset:3072
	ds_read_b128 v[8:11], v155 offset:32768
	ds_read_b128 v[12:15], v155 offset:33792
	ds_read_b128 v[24:27], v155 offset:34816
	ds_read_b128 v[28:31], v155 offset:35840
	ds_read_b128 v[32:35], v155 offset:36864
	ds_read_b128 v[36:39], v155 offset:37888
	ds_read_b128 v[40:43], v155 offset:38912
	ds_read_b128 v[44:47], v155 offset:39936
	s_add_u32 s26, s36, 0xe0000
	s_addc_u32 s27, s37, 0
	s_add_i32 m0, s44, 0x4000
	s_nop 0
	global_load_lds_dwordx4 v149, s[26:27]
	s_nop 0
	s_add_i32 m0, s44, 0x6000
	s_nop 0
	global_load_lds_dwordx4 v151, s[26:27]
	s_waitcnt vmcnt(8) lgkmcnt(0)
	s_barrier
	v_mfma_f32_16x16x128_f8f6f4 v[112:115], v[0:7], v[8:15], v[112:115]
	v_mfma_f32_16x16x128_f8f6f4 v[116:119], v[16:23], v[8:15], v[116:119]
	v_mfma_f32_16x16x128_f8f6f4 v[96:99], v[16:23], v[24:31], v[96:99]
	v_mfma_f32_16x16x128_f8f6f4 v[100:103], v[0:7], v[24:31], v[100:103]
	v_mfma_f32_16x16x128_f8f6f4 v[84:87], v[0:7], v[32:39], v[206:209]
	v_mfma_f32_16x16x128_f8f6f4 v[80:83], v[16:23], v[32:39], v[210:213]
	v_mfma_f32_16x16x128_f8f6f4 v[52:55], v[16:23], v[40:47], v[218:221]
	v_mfma_f32_16x16x128_f8f6f4 v[60:63], v[0:7], v[40:47], v[214:217]
	v_mfma_f32_16x16x128_f8f6f4 v[120:123], v[132:139], v[8:15], v[120:123]
	v_mfma_f32_16x16x128_f8f6f4 v[124:127], v[140:147], v[8:15], v[124:127]
	v_mfma_f32_16x16x128_f8f6f4 v[104:107], v[140:147], v[24:31], v[104:107]
	v_mfma_f32_16x16x128_f8f6f4 v[108:111], v[132:139], v[24:31], v[108:111]
	v_mfma_f32_16x16x128_f8f6f4 v[92:95], v[132:139], v[32:39], v[174:177]
	v_mfma_f32_16x16x128_f8f6f4 v[88:91], v[140:147], v[32:39], v[178:181]
	v_mfma_f32_16x16x128_f8f6f4 v[48:51], v[140:147], v[40:47], v[186:189]
	v_mfma_f32_16x16x128_f8f6f4 v[56:59], v[132:139], v[40:47], v[182:185]
	s_barrier
	ds_read_b128 v[158:161], v155 offset:49152
	ds_read_b128 v[162:165], v155 offset:50176
	ds_read_b128 v[166:169], v155 offset:51200
	ds_read_b128 v[170:173], v155 offset:52224
	ds_read_b128 v[174:177], v155 offset:53248
	ds_read_b128 v[178:181], v155 offset:54272
	ds_read_b128 v[182:185], v155 offset:55296
	ds_read_b128 v[186:189], v155 offset:56320
	s_add_i32 m0, s44, 0x18000
	s_nop 0
	global_load_lds_dwordx4 v150, s[34:35]
	s_nop 0
	s_add_i32 m0, s44, 0x1a000
	s_nop 0
	global_load_lds_dwordx4 v152, s[34:35]
	s_add_u32 s26, s30, 0xe0080
	s_addc_u32 s27, s31, 0
	s_add_i32 m0, s44, 0x1c000
	s_nop 0
	global_load_lds_dwordx4 v150, s[26:27]
	s_nop 0
	s_add_i32 m0, s44, 0x1e000
	s_nop 0
	global_load_lds_dwordx4 v152, s[26:27]
	s_nop 0
	s_add_i32 m0, s44, 0x8000
	s_nop 0
	global_load_lds_dwordx4 v149, s[28:29]
	s_nop 0
	s_add_i32 m0, s44, 0xa000
	s_nop 0
	global_load_lds_dwordx4 v151, s[28:29]
	s_add_i32 s52, s52, 2
	s_add_u32 s23, s23, 0x100
	s_addc_u32 s51, s51, 0
	s_cmp_gt_u32 s52, 53
	s_mov_b64 s[26:27], s[24:25]
	s_waitcnt vmcnt(8) lgkmcnt(0)
	s_barrier
	v_mfma_f32_16x16x128_f8f6f4 v[68:71], v[0:7], v[158:165], v[68:71]
	v_mfma_f32_16x16x128_f8f6f4 v[64:67], v[16:23], v[158:165], v[64:67]
	v_mfma_f32_16x16x128_f8f6f4 v[36:39], v[16:23], v[166:173], v[194:197]
	v_mfma_f32_16x16x128_f8f6f4 v[44:47], v[0:7], v[166:173], v[190:193]
	v_mfma_f32_16x16x128_f8f6f4 v[28:31], v[0:7], v[174:181], v[198:201]
	v_mfma_f32_16x16x128_f8f6f4 v[24:27], v[16:23], v[174:181], v[202:205]
	v_mfma_f32_16x16x128_f8f6f4 v[8:11], v[16:23], v[182:189], v[226:229]
	v_mfma_f32_16x16x128_f8f6f4 v[12:15], v[0:7], v[182:189], v[222:225]
	v_mfma_f32_16x16x128_f8f6f4 v[76:79], v[132:139], v[158:165], v[76:79]
	v_mfma_f32_16x16x128_f8f6f4 v[72:75], v[140:147], v[158:165], v[72:75]
	v_mfma_f32_16x16x128_f8f6f4 v[32:35], v[140:147], v[166:173], v[234:237]
	v_mfma_f32_16x16x128_f8f6f4 v[40:43], v[132:139], v[166:173], v[230:233]
	v_mfma_f32_16x16x128_f8f6f4 v[20:23], v[132:139], v[174:181], v[238:241]
	v_mfma_f32_16x16x128_f8f6f4 v[16:19], v[140:147], v[174:181], v[242:245]
	v_mfma_f32_16x16x128_f8f6f4 v[0:3], v[140:147], v[182:189], v[250:253]
	v_mfma_f32_16x16x128_f8f6f4 v[4:7], v[132:139], v[182:189], v[246:249]
	s_barrier
	s_cbranch_scc0 .LBB0_1488
	s_and_b64 vcc, exec, s[16:17]
	s_cbranch_vccz .LBB0_1491
	s_barrier
